# int8 weight copies (in-proj, gate, MLP-up) stored K-tile-major in LDS-image order; B-side LDS-DMA pieces of G1/G3/G5 read 1 KB contiguous (linear voffsets, re-stepped soffsets)
# speedup vs baseline: 1.0161x; 1.0037x over previous
; __device__ __forceinline__ unsigned char* launder(unsigned char* p) { asm volatile("" : "+s"(p)); return p; }
; #define WSP(T, off) ((T*)(launder(args.ws) + (off)))
; __global__ void __launch_bounds__(NWAVES * 64, 2) mega_fwd(Args args) {
;     ...
;               const float cm = __uint_as_float(cmb), inv = cm > 0.f ? 127.f / cm : 0.f;
;               unsigned char* wq = launder(args.ws) + (which == 0 ? WS_WQIN : (which == 1 ? WS_WQG : WS_WQ1)) + ((size_t)l * nrows + n) * 1024;
; #pragma unroll
;               for (int j = 0; j < 4; ++j) { unsigned pk = 0u;
; #pragma unroll
;                   for (int e = 0; e < 4; ++e) pk |= ((unsigned)(int)__builtin_rintf(w[4 * j + e] * inv) & 255u) << (8 * e);
;                   *(unsigned*)(wq + 256 * j + lane * 4) = pk; }
;               if (lane == 0) WSP(float, WS_SB)[grp * 4096 + n] = cm * (1.f / 127.f); }
.LBB0_295:
	v_div_scale_f32 v34, s[30:31], v33, v33, s23
	v_rcp_f32_e32 v35, v34
	v_cvt_f32_f16_sdwa v31, v22 dst_sel:DWORD dst_unused:UNUSED_PAD src0_sel:WORD_1
	v_cvt_f32_f16_e32 v28, v22
	v_cvt_f32_f16_e32 v29, v23
	v_fma_f32 v36, -v34, v35, 1.0
	v_fmac_f32_e32 v35, v36, v35
	v_div_scale_f32 v36, vcc, s23, v33, s23
	v_mul_f32_e32 v37, v36, v35
	v_fma_f32 v38, -v34, v37, v36
	v_fmac_f32_e32 v37, v38, v35
	v_fma_f32 v34, -v34, v37, v36
	v_div_fmas_f32 v34, v34, v35, v37
	v_div_fixup_f32 v34, v34, v33, s23
	v_cmp_lt_f32_e32 vcc, 0, v33
	v_cvt_f32_f16_sdwa v32, v23 dst_sel:DWORD dst_unused:UNUSED_PAD src0_sel:WORD_1
	v_cvt_f32_f16_sdwa v30, v20 dst_sel:DWORD dst_unused:UNUSED_PAD src0_sel:WORD_1
	v_cndmask_b32_e32 v36, 0, v34, vcc
	v_mul_f32_e32 v38, v36, v31
	v_mul_f32_e32 v37, v36, v28
	v_rndne_f32_e32 v38, v38
	v_rndne_f32_e32 v37, v37
	v_cvt_i32_f32_e32 v38, v38
	v_mul_f32_e32 v39, v36, v29
	v_cvt_i32_f32_e32 v37, v37
	v_rndne_f32_e32 v39, v39
	v_mul_f32_e32 v40, v36, v32
	v_cvt_i32_f32_sdwa v39, v39 dst_sel:WORD_1 dst_unused:UNUSED_PAD src0_sel:DWORD
	v_rndne_f32_e32 v40, v40
	v_cvt_i32_f32_e32 v40, v40
	v_cvt_f32_f16_e32 v26, v20
	v_lshlrev_b32_e32 v38, 8, v38
	v_cvt_f32_f16_e32 v25, v21
	v_readlane_b32 s30, v253, 54
	v_perm_b32 v37, v38, v37, s34
	v_cvt_f32_f16_sdwa v27, v21 dst_sel:DWORD dst_unused:UNUSED_PAD src0_sel:WORD_1
	v_readlane_b32 s31, v253, 55
	v_and_or_b32 v37, v39, s35, v37
	v_lshl_or_b32 v37, v40, 24, v37
	v_bfe_u32 v56, v6, 10, 7
	v_bfe_u32 v57, v6, 17, 1
	v_and_b32_e32 v58, 3, v56
	v_bfe_u32 v59, v56, 3, 2
	v_lshl_or_b32 v58, v59, 2, v58
	v_bfe_u32 v59, v56, 2, 1
	v_lshl_or_b32 v58, v59, 4, v58
	v_and_b32_e32 v59, 0x60, v56
	v_or_b32_e32 v58, v59, v58
	v_bfe_u32 v60, v6, 2, 6
	v_lshrrev_b32_e32 v59, 4, v58
	v_bfe_u32 v61, v60, 4, 1
	v_lshl_or_b32 v59, v59, 1, v61
	v_and_b32_e32 v61, 15, v60
	v_lshlrev_b32_e32 v61, 2, v61
	v_bfe_u32 v62, v58, 3, 1
	v_lshlrev_b32_e32 v62, 5, v62
	v_xor_b32_e32 v61, v61, v62
	v_and_b32_e32 v62, 15, v58
	v_lshl_or_b32 v61, v62, 6, v61
	v_lshl_or_b32 v61, v59, 10, v61
	v_lshl_or_b32 v61, v57, 14, v61
	v_bfe_u32 v62, v60, 5, 1
	v_lshl_or_b32 v61, v62, 15, v61
	v_and_b32_e32 v62, 0xfffc0000, v6
	v_or_b32_e32 v62, v62, v61
	v_mov_b32_e32 v63, v7
	v_lshl_add_u64 v[34:35], s[30:31], 0, v[62:63]
	s_mov_b64 s[100:101], 0x10000
	v_lshl_add_u64 v[64:65], v[34:35], 0, s[100:101]
	v_lshl_add_u64 v[66:67], v[64:65], 0, s[100:101]
	v_lshl_add_u64 v[68:69], v[66:67], 0, s[100:101]
	v_mul_f32_e32 v38, v36, v30
	flat_store_dword v[34:35], v37
	v_mul_f32_e32 v37, v36, v26
	v_rndne_f32_e32 v38, v38
	v_rndne_f32_e32 v37, v37
	v_cvt_i32_f32_e32 v38, v38
	v_mul_f32_e32 v39, v36, v25
	v_cvt_i32_f32_e32 v37, v37
	v_rndne_f32_e32 v39, v39
	v_mul_f32_e32 v40, v36, v27
	v_cvt_i32_f32_sdwa v39, v39 dst_sel:WORD_1 dst_unused:UNUSED_PAD src0_sel:DWORD
	v_rndne_f32_e32 v40, v40
	v_cvt_f32_f16_sdwa v22, v18 dst_sel:DWORD dst_unused:UNUSED_PAD src0_sel:WORD_1
	v_cvt_i32_f32_e32 v40, v40
	v_cvt_f32_f16_e32 v20, v18
	v_lshlrev_b32_e32 v38, 8, v38
	v_cvt_f32_f16_e32 v21, v19
	v_perm_b32 v37, v38, v37, s34
	v_cvt_f32_f16_sdwa v19, v19 dst_sel:DWORD dst_unused:UNUSED_PAD src0_sel:WORD_1
	v_and_or_b32 v37, v39, s35, v37
	v_lshl_or_b32 v37, v40, 24, v37
	v_mul_f32_e32 v38, v36, v22
	flat_store_dword v[64:65], v37
	v_mul_f32_e32 v37, v36, v20
	v_rndne_f32_e32 v38, v38
	v_rndne_f32_e32 v37, v37
	v_cvt_i32_f32_e32 v38, v38
	v_mul_f32_e32 v39, v36, v21
	v_cvt_i32_f32_e32 v37, v37
	v_rndne_f32_e32 v39, v39
	v_mul_f32_e32 v40, v36, v19
	v_cvt_i32_f32_sdwa v39, v39 dst_sel:WORD_1 dst_unused:UNUSED_PAD src0_sel:DWORD
	v_rndne_f32_e32 v40, v40
	v_cvt_f32_f16_sdwa v23, v16 dst_sel:DWORD dst_unused:UNUSED_PAD src0_sel:WORD_1
	v_cvt_i32_f32_e32 v40, v40
	v_cvt_f32_f16_e32 v18, v16
	v_lshlrev_b32_e32 v38, 8, v38
	v_cvt_f32_f16_e32 v16, v17
	v_perm_b32 v37, v38, v37, s34
	v_cvt_f32_f16_sdwa v17, v17 dst_sel:DWORD dst_unused:UNUSED_PAD src0_sel:WORD_1
	v_and_or_b32 v37, v39, s35, v37
	v_lshl_or_b32 v37, v40, 24, v37
	v_mul_f32_e32 v38, v36, v23
	flat_store_dword v[66:67], v37
	v_mul_f32_e32 v37, v36, v18
	v_rndne_f32_e32 v38, v38
	v_rndne_f32_e32 v37, v37
	v_cvt_i32_f32_e32 v38, v38
	v_mul_f32_e32 v39, v36, v16
	v_cvt_i32_f32_e32 v37, v37
	v_rndne_f32_e32 v39, v39
	v_mul_f32_e32 v36, v36, v17
	v_cvt_i32_f32_sdwa v39, v39 dst_sel:WORD_1 dst_unused:UNUSED_PAD src0_sel:DWORD
	v_rndne_f32_e32 v36, v36
	v_cvt_i32_f32_e32 v36, v36
	v_lshlrev_b32_e32 v38, 8, v38
	v_perm_b32 v37, v38, v37, s34
	v_and_or_b32 v37, v39, s35, v37
	v_lshl_or_b32 v36, v36, 24, v37
	flat_store_dword v[68:69], v36
	s_and_saveexec_b64 s[30:31], s[8:9]
	s_cbranch_execz .LBB0_297
	v_readlane_b32 s36, v253, 54
	s_ashr_i32 s21, s20, 31
	v_readlane_b32 s37, v253, 55
	s_lshl_b64 s[38:39], s[20:21], 2
	s_add_u32 s1, s36, s38
	s_addc_u32 s7, s37, s39
	v_mov_b32_e32 v34, s1
	v_add_co_u32_e32 v34, vcc, 0x3c0000, v34
	v_mov_b32_e32 v35, s7
	v_mul_f32_e32 v33, 0x3c010204, v33
	v_addc_co_u32_e32 v35, vcc, 0, v35, vcc
	flat_store_dword v[34:35], v33

;     __host__ __device__ bool next(int i, Unit& u) const { if (!so.next(i / 3, u)) return false; u.pn += 4 * (i % 3); u.idx = i; return true; }
; #define PG8_BAR __builtin_amdgcn_s_barrier()
; template <class Epi, class Sched, bool ALIGN_EPI = false, bool SP2 = false, bool I8 = false, bool ATILED = false>
; __device__ __forceinline__ void gemm_phase(PG8_LAS unsigned char* lds, const Gemm g, const Sched& S, const Epi& E, const int wid) {
;     ...
;     for (int i = 0; i < 2; ++i) { int R, C; stage_rc(tid * 16 + i * 8192, R, C); const int Rb = Epi::PERM ? ((R & ~31) + perm32(R & 31)) : R;
;         voffA[i] = (unsigned)(R * (ATILED ? BK : K) + C) * 2u; voffB[i] = (unsigned)(Rb * K + C) * 2u; }
;     const unsigned kstep = (unsigned)(BK * 2);
;     const unsigned hstep = (unsigned)HALF * K * 2;
;     const unsigned tstep = 2 * hstep;
;     const unsigned kstepA = ATILED ? (unsigned)(BM * BK * 2) : kstep, hstepA = ATILED ? (unsigned)(HALF * BK * 2) : hstep, tstepA = ATILED ? (unsigned)nt * (unsigned)(BM * BK * 2) : tstep;
;     const __amdgpu_buffer_rsrc_t rsA = __builtin_amdgcn_make_buffer_rsrc((void*)g.A, 0, 0x7fffffff, 0x00020000), rsB = __builtin_amdgcn_make_buffer_rsrc((void*)g.Bt, 0, 0x7fffffff, 0x00020000);
;     const unsigned ldsw = (unsigned)wid * 1024u;
;     const int aoff = lds_byte(wr * 64 + fr, fq * 8), boff = lds_byte(wc * 32 + fr, fq * 8);
;     ...
;     Unit cur, nxt; int ui = 0;
;     if (!S.next(0, cur)) return;
;     f32x4 acc[2][2][4][2];
; #pragma unroll
;     for (int a = 0; a < 2; ++a)
; #pragma unroll
;         for (int b = 0; b < 2; ++b)
; #pragma unroll
;             for (int m = 0; m < 4; ++m)
; #pragma unroll
;                 for (int n = 0; n < 2; ++n) acc[a][b][m][n] = (f32x4){0.f, 0.f, 0.f, 0.f};
;     f16x8 At[4][2], B0[2][2], B1[2][2];
;     unsigned cA = (unsigned)cur.pm * tstepA + (unsigned)(cur.pm >> 4) * g.gapA, cB = (unsigned)cur.pn * tstep;
;     S.a_ready(cur);
;     if constexpr (SP2) {
;         PG8_STAGE(PG8_SB(0, 0), rsB, cB, voffB); PG8_STAGE(PG8_SB(0, 1), rsB, cB + hstep, voffB); PG8_STAGE(PG8_SA(0, 0), rsA, cA, voffA); PG8_STAGE(PG8_SA(0, 1), rsA, cA + hstepA, voffA);
;         if (wr == 1) PG8_BAR;
;         PG8_WAIT_V(2); PG8_BAR;
;         PG8_STAGE(PG8_SB(1, 0), rsB, cB + kstep, voffB); PG8_STAGE(PG8_SA(1, 0), rsA, cA + kstepA, voffA); PG8_STAGE(PG8_SB(1, 1), rsB, cB + hstep + kstep, voffB);
;         PG8_WAIT_V(6); PG8_BAR;
.LBB0_474:
	v_readlane_b32 s28, v253, 63
	v_readlane_b32 s29, v254, 0
	s_andn2_b64 vcc, exec, s[28:29]
	v_readlane_b32 s28, v254, 1
	v_readlane_b32 s29, v254, 2
	s_waitcnt lgkmcnt(0)
	s_barrier
	v_cndmask_b32_e64 v0, 0, 1, s[28:29]
	v_cmp_ne_u32_e64 s[22:23], 1, v0
	v_mbcnt_lo_u32_b32 v2, -1, 0
	v_mbcnt_hi_u32_b32 v2, -1, v2
	s_nop 1
	v_writelane_b32 v253, s22, 31
	s_nop 1
	v_writelane_b32 v253, s23, 32
	s_cbranch_vccnz .LBB0_490
	v_lshl_add_u32 v3, v2, 4, s85
	v_ashrrev_i32_e32 v0, 31, v3
	v_lshrrev_b32_e32 v0, 22, v0
	v_add_u32_e32 v0, v3, v0
	v_ashrrev_i32_e32 v0, 10, v0
	s_waitcnt vmcnt(0)
	v_mul_i32_i24_e32 v4, 0x400, v0
	v_sub_u32_e32 v4, v3, v4
	v_lshrrev_b32_e32 v5, 4, v4
	v_bitop3_b32 v4, v5, v4, 32 bitop3:0x6c
	v_ashrrev_i32_e32 v6, 31, v4
	s_mul_hi_i32 s27, s26, 0x340000
	s_mul_i32 s26, s26, 0x340000
	v_lshrrev_b32_e32 v6, 26, v6
	s_add_u32 s26, s42, s26
	v_lshlrev_b32_e32 v5, 3, v0
	v_add_u32_e32 v6, v4, v6
	s_addc_u32 s27, s43, s27
	v_and_b32_e32 v5, -16, v5
	v_ashrrev_i32_e32 v7, 6, v6
	v_and_b32_e32 v6, 0xc0, v6
	s_add_u32 s64, s26, 0x1f000000
	v_add_u32_e32 v5, v7, v5
	v_sub_u32_e32 v4, v4, v6
	s_addc_u32 s26, s27, 0
	v_lshlrev_b32_e32 v0, 5, v0
	v_ashrrev_i16_sdwa v4, v232, sext(v4) dst_sel:DWORD dst_unused:UNUSED_PAD src0_sel:DWORD src1_sel:BYTE_0
	v_lshlrev_b32_e32 v6, 1, v5
	v_lshrrev_b32_e32 v8, 2, v5
	v_and_b32_e32 v7, 3, v7
	s_mov_b32 s27, 0x3fffe0
	v_and_b32_e32 v0, 32, v0
	v_bfe_i32 v4, v4, 0, 16
	v_and_b32_e32 v6, 24, v6
	v_and_b32_e32 v8, 4, v8
	v_and_or_b32 v7, v5, s27, v7
	v_or3_b32 v6, v7, v8, v6
	v_add_lshl_u32 v4, v0, v4, 1
	v_add_u32_e32 v3, 0x2000, v3
	v_lshl_add_u32 v0, v5, 10, v4
	v_mbcnt_lo_u32_b32 v172, -1, 0
	v_mbcnt_hi_u32_b32 v172, -1, v172
	v_lshl_add_u32 v172, v172, 4, s85
	v_ashrrev_i32_e32 v4, 31, v3
	v_lshrrev_b32_e32 v4, 22, v4
	v_add_u32_e32 v4, v3, v4
	v_ashrrev_i32_e32 v4, 10, v4
	v_mul_i32_i24_e32 v5, 0x400, v4
	v_sub_u32_e32 v3, v3, v5
	v_lshrrev_b32_e32 v5, 4, v3
	v_bitop3_b32 v3, v5, v3, 32 bitop3:0x6c
	v_ashrrev_i32_e32 v6, 31, v3
	v_lshrrev_b32_e32 v6, 26, v6
	v_add_u32_e32 v6, v3, v6
	v_ashrrev_i32_e32 v7, 6, v6
	v_and_b32_e32 v6, 0xffc0, v6
	v_sub_u32_e32 v3, v3, v6
	v_lshlrev_b32_e32 v5, 3, v4
	v_lshrrev_b16_e32 v6, 7, v3
	v_and_b32_e32 v5, -16, v5
	v_and_b32_e32 v6, 1, v6
	v_add_u32_e32 v5, v7, v5
	v_add_u16_e32 v3, v3, v6
	s_and_b32 s65, s26, 0xffff
	s_mov_b32 s26, s85
	v_lshlrev_b32_e32 v4, 5, v4
	v_ashrrev_i16_sdwa v3, v232, sext(v3) dst_sel:DWORD dst_unused:UNUSED_PAD src0_sel:DWORD src1_sel:BYTE_0
	v_lshlrev_b32_e32 v6, 1, v5
	v_lshrrev_b32_e32 v8, 2, v5
	v_and_b32_e32 v7, 3, v7
	v_and_b32_e32 v4, 32, v4
	v_bfe_i32 v3, v3, 0, 16
	v_and_b32_e32 v6, 24, v6
	v_and_b32_e32 v8, 4, v8
	v_and_or_b32 v7, v5, s27, v7
	s_add_i32 m0, s26, 0x10000
	v_readlane_b32 s27, v254, 29
	s_bfe_u32 s100, s27, 0x10011
	s_bfe_u32 s101, s27, 0x10007
	s_and_b32 s27, s27, 0xfffc0000
	s_lshl_b32 s100, s100, 14
	s_lshl_b32 s101, s101, 15
	s_or_b32 s27, s27, s100
	s_or_b32 s27, s27, s101
	s_mov_b32 s26, s85
	v_or3_b32 v6, v7, v8, v6
	v_add_lshl_u32 v3, v4, v3, 1
	v_mbcnt_lo_u32_b32 v174, -1, 0
	v_mbcnt_hi_u32_b32 v174, -1, v174
	v_lshl_add_u32 v174, v174, 4, s85
	v_add_u32_e32 v174, 0x2000, v174
	s_mov_b32 s90, s66
	buffer_load_dwordx4 v172, s[64:67], s27 offen lds
	s_add_i32 m0, s26, 0x12000
	s_mov_b32 s26, s85
	buffer_load_dwordx4 v174, s[64:67], s27 offen lds
	s_add_i32 m0, s26, 0x14000
	v_readlane_b32 s27, v254, 23
	s_bfe_u32 s100, s27, 0x10011
	s_bfe_u32 s101, s27, 0x10007
	s_and_b32 s27, s27, 0xfffc0000
	s_lshl_b32 s100, s100, 14
	s_lshl_b32 s101, s101, 15
	s_or_b32 s27, s27, s100
	s_or_b32 s27, s27, s101
	s_mov_b32 s26, s85
	s_mov_b32 s91, s67
	v_lshl_add_u32 v173, v5, 10, v3
	v_readlane_b32 s22, v253, 31
	v_readlane_b32 s23, v253, 32
	buffer_load_dwordx4 v172, s[64:67], s27 offen lds
	s_add_i32 m0, s26, 0x16000
	s_mov_b32 s26, s85
	buffer_load_dwordx4 v174, s[64:67], s27 offen lds
	s_mov_b32 m0, s26
	v_readlane_b32 s27, v254, 27
	s_mov_b32 s26, s85
	s_and_b64 vcc, exec, s[22:23]
	s_nop 2
	buffer_load_dwordx4 v0, s[88:91], s27 offen lds
	s_add_i32 m0, s26, 0x2000
	s_mov_b32 s26, s85
	buffer_load_dwordx4 v173, s[88:91], s27 offen lds
	s_add_i32 m0, s26, 0x4000
	v_readlane_b32 s27, v254, 25
	s_mov_b32 s26, s85
	s_nop 3
	buffer_load_dwordx4 v0, s[88:91], s27 offen lds
	s_add_i32 m0, s26, 0x6000
	s_nop 0
	buffer_load_dwordx4 v173, s[88:91], s27 offen lds
	s_cbranch_vccnz .LBB0_477
	s_barrier
.LBB0_477:
	s_mov_b32 s26, s85
	s_add_u32 s34, s40, 0xe800000
	s_waitcnt vmcnt(2)
	s_barrier
	s_addc_u32 s35, s41, 0
	s_add_i32 m0, s26, 0x18000
	v_readlane_b32 s27, v254, 26
	s_bfe_u32 s100, s27, 0x10011
	s_bfe_u32 s101, s27, 0x10007
	s_and_b32 s27, s27, 0xfffc0000
	s_lshl_b32 s100, s100, 14
	s_lshl_b32 s101, s101, 15
	s_or_b32 s27, s27, s100
	s_or_b32 s27, s27, s101
	s_mov_b32 s26, s85
	v_and_b32_e32 v175, 15, v2
	v_or_b32_e32 v176, s96, v175
	v_lshlrev_b32_e32 v5, 6, v176
	v_and_b32_e32 v6, 48, v2
	buffer_load_dwordx4 v172, s[64:67], s27 offen lds
	s_add_i32 m0, s26, 0x1a000
	s_mov_b32 s26, s85
	buffer_load_dwordx4 v174, s[64:67], s27 offen lds
	s_add_i32 m0, s26, 0x8000
	v_readlane_b32 s27, v254, 28
	s_mov_b32 s26, s85
	v_ashrrev_i32_e32 v4, 6, v2
	v_ashrrev_i32_e32 v3, 1, v2
	v_lshlrev_b32_e32 v8, 2, v176
	v_and_b32_e32 v3, -8, v3
	buffer_load_dwordx4 v0, s[88:91], s27 offen lds
	s_add_i32 m0, s26, 0xa000
	s_mov_b32 s26, s85
	buffer_load_dwordx4 v173, s[88:91], s27 offen lds
	s_add_i32 m0, s26, 0x1c000
	v_readlane_b32 s27, v254, 30
	s_bfe_u32 s100, s27, 0x10011
	s_bfe_u32 s101, s27, 0x10007
	s_and_b32 s27, s27, 0xfffc0000
	s_lshl_b32 s100, s100, 14
	s_lshl_b32 s101, s101, 15
	s_or_b32 s27, s27, s100
	s_or_b32 s27, s27, s101
	s_mov_b32 s26, s85
	v_and_b32_e32 v8, 32, v8
	v_lshlrev_b32_e32 v2, 2, v2
	v_and_b32_e32 v2, 32, v2
	s_mov_b32 s44, 0
	buffer_load_dwordx4 v172, s[64:67], s27 offen lds
	s_add_i32 m0, s26, 0x1e000
	s_movk_i32 s26, 0x3c0
	buffer_load_dwordx4 v174, s[64:67], s27 offen lds
	v_and_or_b32 v5, v5, s26, v6
	v_readlane_b32 s26, v253, 60
	s_waitcnt vmcnt(6)
	v_readlane_b32 s42, v254, 22
	v_readlane_b32 s43, v254, 24
	v_lshl_add_u32 v7, v4, 10, s26
	v_readlane_b32 s26, v253, 62
	v_bitop3_b32 v177, v5, v7, v8 bitop3:0xde
	v_lshl_or_b32 v5, v175, 6, v6
	v_add_lshl_u32 v4, v4, s26, 10
	v_readlane_b32 s26, v253, 61
	v_bitop3_b32 v178, v5, v4, v2 bitop3:0xde
	v_readlane_b32 s48, v254, 29
	v_add_u32_e32 v179, s26, v3
	v_lshlrev_b32_e32 v2, 2, v179
	v_add_u32_e32 v180, 0x22400, v2
	v_add_u32_e32 v181, 0x24400, v2
	v_readlane_b32 s47, v254, 27
	s_mov_b32 s49, 0
	s_barrier
	s_branch .LBB0_480

;     __host__ __device__ bool next(int i, Unit& u) const { if (!so.next(i / 3, u)) return false; u.pn += 4 * (i % 3); u.idx = i; return true; }
; #define PG8_STAGE(bufoff, RS, soff, voff) do { _Pragma("unroll") for (int _i = 0; _i < 2; ++_i) \
;         __builtin_amdgcn_raw_ptr_buffer_load_lds(RS, (PG8_LAS void*)(lds + (bufoff) + sgpr_opaque(ldsw) + _i * 8192), 16, (int)(voff)[_i], (int)(soff), 0, 0); } while (0)
; #define PG8_LDA(dst, b, h) do { _Pragma("unroll") for (int m = 0; m < 4; ++m) _Pragma("unroll") for (int k = 0; k < 2; ++k) dst[m][k] = *(const PG8_LAS f16x8*)(lds + PG8_SA(b, h) + aoff + m * 2048 + k * 1024); } while (0)
; #define PG8_LDB(dst, b, h) do { _Pragma("unroll") for (int n = 0; n < 2; ++n) _Pragma("unroll") for (int k = 0; k < 2; ++k) dst[n][k] = *(const PG8_LAS f16x8*)(lds + PG8_SB(b, h) + boff + n * 2048 + k * 1024); } while (0)
; template <class Epi, class Sched, bool ALIGN_EPI = false, bool SP2 = false, bool I8 = false, bool ATILED = false>
; __device__ __forceinline__ void gemm_phase(PG8_LAS unsigned char* lds, const Gemm g, const Sched& S, const Epi& E, const int wid) {
;     ...
;         const bool has_next = S.next(ui + 1, nxt);
;         const unsigned nA = has_next ? (unsigned)nxt.pm * tstepA + (unsigned)(nxt.pm >> 4) * g.gapA : cA, nB = has_next ? (unsigned)nxt.pn * tstep : cB;
;         for (int t = 0; t < nt; t += 2) {
;             const bool last = (t == nt - 2);
;             const unsigned a1 = cA + (unsigned)(t + 1) * kstepA;
;             const unsigned a2 = last ? nA : cA + (unsigned)(t + 2) * kstepA, b2 = last ? nB : cB + (unsigned)(t + 2) * kstep;
;             const unsigned a3 = a2 + kstepA, b3 = b2 + kstep;
;             if (last && has_next) S.a_ready(nxt);
;             if constexpr (SP2) {
;             const int grace = __builtin_amdgcn_readfirstlane((PG8_GRACE && Epi::NSTORE > 0 && t == 0 && ui > 0) ? 1 : 0);
;     ...
;             PG8_LDB(B0, 0, 0); PG8_LDB(B1, 0, 1); PG8_SCHED; PG8_LDA(At, 0, 0); PG8_STAGE(PG8_SA(1, 1), rsA, a1 + hstepA, voffA);
;     ...
; #pragma unroll
;         for (int a = 0; a < 2; ++a)
; #pragma unroll
;             for (int b = 0; b < 2; ++b)
; #pragma unroll
;                 for (int m = 0; m < 4; ++m)
; #pragma unroll
;                     for (int n = 0; n < 2; ++n) acc[a][b][m][n] = (f32x4){0.f, 0.f, 0.f, 0.f};
;         cur = nxt; cA = nA; cB = nB; ++ui;
.LBB0_482:
	s_lshl_b32 s40, s39, 18
	s_and_b64 s[36:37], s[30:31], exec
	s_cselect_b32 s45, s40, s47
	s_lshl_b32 s41, s27, 18
	s_and_b64 s[36:37], s[30:31], exec
	s_cselect_b32 s46, s41, s48
	s_cmp_lg_u32 s49, 0
	v_mov_b32_e32 v2, 0
	s_cselect_b64 s[36:37], -1, 0
	s_add_i32 s47, s47, 0x20080
	s_add_i32 s48, s48, 0x10000
	s_mov_b32 s49, -2
	v_mov_b32_e32 v3, v2
	v_mov_b32_e32 v4, v2
	v_mov_b32_e32 v5, v2
	v_mov_b32_e32 v6, v2
	v_mov_b32_e32 v7, v2
	v_mov_b32_e32 v8, v2
	v_mov_b32_e32 v9, v2
	v_mov_b32_e32 v18, v2
	v_mov_b32_e32 v19, v2
	v_mov_b32_e32 v20, v2
	v_mov_b32_e32 v21, v2
	v_mov_b32_e32 v22, v2
	v_mov_b32_e32 v23, v2
	v_mov_b32_e32 v24, v2
	v_mov_b32_e32 v25, v2
	v_mov_b32_e32 v34, v2
	v_mov_b32_e32 v35, v2
	v_mov_b32_e32 v36, v2
	v_mov_b32_e32 v37, v2
	v_mov_b32_e32 v38, v2
	v_mov_b32_e32 v39, v2
	v_mov_b32_e32 v40, v2
	v_mov_b32_e32 v41, v2
	v_mov_b32_e32 v50, v2
	v_mov_b32_e32 v51, v2
	v_mov_b32_e32 v52, v2
	v_mov_b32_e32 v53, v2
	v_mov_b32_e32 v54, v2
	v_mov_b32_e32 v55, v2
	v_mov_b32_e32 v56, v2
	v_mov_b32_e32 v57, v2
	v_mov_b32_e32 v10, v2
	v_mov_b32_e32 v11, v2
	v_mov_b32_e32 v12, v2
	v_mov_b32_e32 v13, v2
	v_mov_b32_e32 v14, v2
	v_mov_b32_e32 v15, v2
	v_mov_b32_e32 v16, v2
	v_mov_b32_e32 v17, v2
	v_mov_b32_e32 v26, v2
	v_mov_b32_e32 v27, v2
	v_mov_b32_e32 v28, v2
	v_mov_b32_e32 v29, v2
	v_mov_b32_e32 v30, v2
	v_mov_b32_e32 v31, v2
	v_mov_b32_e32 v32, v2
	v_mov_b32_e32 v33, v2
	v_mov_b32_e32 v42, v2
	v_mov_b32_e32 v43, v2
	v_mov_b32_e32 v44, v2
	v_mov_b32_e32 v45, v2
	v_mov_b32_e32 v46, v2
	v_mov_b32_e32 v47, v2
	v_mov_b32_e32 v48, v2
	v_mov_b32_e32 v49, v2
	v_mov_b32_e32 v58, v2
	v_mov_b32_e32 v59, v2
	v_mov_b32_e32 v60, v2
	v_mov_b32_e32 v61, v2
	v_mov_b32_e32 v62, v2
	v_mov_b32_e32 v63, v2
	v_mov_b32_e32 v64, v2
	v_mov_b32_e32 v65, v2
	v_mov_b32_e32 v66, v2
	v_mov_b32_e32 v67, v2
	v_mov_b32_e32 v68, v2
	v_mov_b32_e32 v69, v2
	v_mov_b32_e32 v70, v2
	v_mov_b32_e32 v71, v2
	v_mov_b32_e32 v72, v2
	v_mov_b32_e32 v73, v2
	v_mov_b32_e32 v82, v2
	v_mov_b32_e32 v83, v2
	v_mov_b32_e32 v84, v2
	v_mov_b32_e32 v85, v2
	v_mov_b32_e32 v86, v2
	v_mov_b32_e32 v87, v2
	v_mov_b32_e32 v88, v2
	v_mov_b32_e32 v89, v2
	v_mov_b32_e32 v98, v2
	v_mov_b32_e32 v99, v2
	v_mov_b32_e32 v100, v2
	v_mov_b32_e32 v101, v2
	v_mov_b32_e32 v102, v2
	v_mov_b32_e32 v103, v2
	v_mov_b32_e32 v104, v2
	v_mov_b32_e32 v105, v2
	v_mov_b32_e32 v114, v2
	v_mov_b32_e32 v115, v2
	v_mov_b32_e32 v116, v2
	v_mov_b32_e32 v117, v2
	v_mov_b32_e32 v118, v2
	v_mov_b32_e32 v119, v2
	v_mov_b32_e32 v120, v2
	v_mov_b32_e32 v121, v2
	v_mov_b32_e32 v74, v2
	v_mov_b32_e32 v75, v2
	v_mov_b32_e32 v76, v2
	v_mov_b32_e32 v77, v2
	v_mov_b32_e32 v78, v2
	v_mov_b32_e32 v79, v2
	v_mov_b32_e32 v80, v2
	v_mov_b32_e32 v81, v2
	v_mov_b32_e32 v90, v2
	v_mov_b32_e32 v91, v2
	v_mov_b32_e32 v92, v2
	v_mov_b32_e32 v93, v2
	v_mov_b32_e32 v94, v2
	v_mov_b32_e32 v95, v2
	v_mov_b32_e32 v96, v2
	v_mov_b32_e32 v97, v2
	v_mov_b32_e32 v106, v2
	v_mov_b32_e32 v107, v2
	v_mov_b32_e32 v108, v2
	v_mov_b32_e32 v109, v2
	v_mov_b32_e32 v110, v2
	v_mov_b32_e32 v111, v2
	v_mov_b32_e32 v112, v2
	v_mov_b32_e32 v113, v2
	v_mov_b32_e32 v122, v2
	v_mov_b32_e32 v123, v2
	v_mov_b32_e32 v124, v2
	v_mov_b32_e32 v125, v2
	v_mov_b32_e32 v126, v2
	v_mov_b32_e32 v127, v2
	v_mov_b32_e32 v128, v2
	v_mov_b32_e32 v129, v2
.LBB0_483:
	s_add_i32 s50, s47, 0xfffe0080
	v_add_u32_e32 v142, 0x10000, v178
	v_add_u32_e32 v158, 0x14000, v178
	s_cmp_eq_u32 s49, 4
	ds_read_b128 v[130:133], v142
	ds_read_b128 v[134:137], v142 offset:1024
	ds_read_b128 v[138:141], v142 offset:2048
	ds_read_b128 v[142:145], v142 offset:3072
	ds_read_b128 v[146:149], v158
	ds_read_b128 v[150:153], v158 offset:1024
	ds_read_b128 v[154:157], v158 offset:2048
	ds_read_b128 v[158:161], v158 offset:3072
	s_cselect_b32 s54, s45, s50
	s_cselect_b32 s51, s46, s48
	s_or_b32 s50, s54, 0x80
	s_cmp_eq_u32 s49, -2
	s_cselect_b64 s[52:53], -1, 0
	s_and_b64 s[52:53], s[36:37], s[52:53]
	v_cndmask_b32_e64 v162, 0, 1, s[52:53]
	s_or_b32 s52, s51, 0x8000
	v_readfirstlane_b32 s53, v162
	s_mov_b32 s55, s85
	ds_read_b128 v[162:165], v177
	ds_read_b128 v[166:169], v177 offset:1024
	ds_read_b128 v[182:185], v177 offset:2048
	ds_read_b128 v[186:189], v177 offset:3072
	ds_read_b128 v[190:193], v177 offset:4096
	ds_read_b128 v[194:197], v177 offset:5120
	ds_read_b128 v[208:211], v177 offset:6144
	ds_read_b128 v[212:215], v177 offset:7168
	s_add_i32 m0, s55, 0xc000
	s_mov_b32 s90, s66
	s_mov_b32 s91, s67
	s_mov_b32 s55, s85
	buffer_load_dwordx4 v0, s[88:91], s47 offen lds
	s_add_i32 m0, s55, 0xe000
	s_and_b32 s53, s53, 1
	buffer_load_dwordx4 v173, s[88:91], s47 offen lds
	s_cmp_lg_u32 s53, 0
	s_cbranch_scc1 .Lgr0
	s_waitcnt vmcnt(8)
; #define PG8_STAGE(bufoff, RS, soff, voff) do { _Pragma("unroll") for (int _i = 0; _i < 2; ++_i) \
;         __builtin_amdgcn_raw_ptr_buffer_load_lds(RS, (PG8_LAS void*)(lds + (bufoff) + sgpr_opaque(ldsw) + _i * 8192), 16, (int)(voff)[_i], (int)(soff), 0, 0); } while (0)
; #define PG8_LDA(dst, b, h) do { _Pragma("unroll") for (int m = 0; m < 4; ++m) _Pragma("unroll") for (int k = 0; k < 2; ++k) dst[m][k] = *(const PG8_LAS f16x8*)(lds + PG8_SA(b, h) + aoff + m * 2048 + k * 1024); } while (0)
; #define PG8_LDB(dst, b, h) do { _Pragma("unroll") for (int n = 0; n < 2; ++n) _Pragma("unroll") for (int k = 0; k < 2; ++k) dst[n][k] = *(const PG8_LAS f16x8*)(lds + PG8_SB(b, h) + boff + n * 2048 + k * 1024); } while (0)
; #define PG8_WAIT_L(n) asm volatile("s_waitcnt lgkmcnt(" #n ")" ::: "memory")
; #define PG8_BAR __builtin_amdgcn_s_barrier()
; #define PG8_SCHED __builtin_amdgcn_sched_barrier(0)
; template <class Epi, class Sched, bool ALIGN_EPI = false, bool SP2 = false, bool I8 = false, bool ATILED = false>
; __device__ __forceinline__ void gemm_phase(PG8_LAS unsigned char* lds, const Gemm g, const Sched& S, const Epi& E, const int wid) {
;     ...
;             PG8_LDB(B0, 0, 0); PG8_LDB(B1, 0, 1); PG8_SCHED; PG8_LDA(At, 0, 0); PG8_STAGE(PG8_SA(1, 1), rsA, a1 + hstepA, voffA);
;             PG8_WAIT_VG; PG8_WAIT_L(0); PG8_BAR; PG8_MMA(0, 0, At, B0); PG8_MMA(0, 1, At, B1); PG8_BAR; PG8_SCHED;
;             PG8_LDA(At, 0, 1); PG8_STAGE(PG8_SB(0, 0), rsB, b2, voffB); PG8_STAGE(PG8_SB(0, 1), rsB, b2 + hstep, voffB); PG8_STAGE(PG8_SA(0, 0), rsA, a2, voffA);
.Lgr0:
	s_waitcnt vmcnt(24)
	s_waitcnt lgkmcnt(0)
	s_barrier
	s_setprio 1
	s_waitcnt lgkmcnt(7)
	v_mfma_i32_16x16x64_i8 v[126:129], v[130:133], v[162:165], v[126:129]
	v_mfma_i32_16x16x64_i8 v[122:125], v[138:141], v[162:165], v[122:125]
	s_waitcnt lgkmcnt(5)
	v_mfma_i32_16x16x64_i8 v[110:113], v[130:133], v[182:185], v[110:113]
	v_mfma_i32_16x16x64_i8 v[106:109], v[138:141], v[182:185], v[106:109]
	s_waitcnt lgkmcnt(3)
	v_mfma_i32_16x16x64_i8 v[94:97], v[130:133], v[190:193], v[94:97]
	v_mfma_i32_16x16x64_i8 v[90:93], v[138:141], v[190:193], v[90:93]
	s_waitcnt lgkmcnt(1)
	v_mfma_i32_16x16x64_i8 v[78:81], v[130:133], v[208:211], v[78:81]
	v_mfma_i32_16x16x64_i8 v[74:77], v[138:141], v[208:211], v[74:77]
	v_mfma_i32_16x16x64_i8 v[126:129], v[134:137], v[166:169], v[126:129]
	v_mfma_i32_16x16x64_i8 v[122:125], v[142:145], v[166:169], v[122:125]
	v_mfma_i32_16x16x64_i8 v[110:113], v[134:137], v[186:189], v[110:113]
	v_mfma_i32_16x16x64_i8 v[106:109], v[142:145], v[186:189], v[106:109]
	v_mfma_i32_16x16x64_i8 v[94:97], v[134:137], v[194:197], v[94:97]
	v_mfma_i32_16x16x64_i8 v[90:93], v[142:145], v[194:197], v[90:93]
	s_waitcnt lgkmcnt(0)
	v_mfma_i32_16x16x64_i8 v[78:81], v[134:137], v[212:215], v[78:81]
	v_mfma_i32_16x16x64_i8 v[74:77], v[142:145], v[212:215], v[74:77]
	s_setprio 0
	s_setprio 1
	v_mfma_i32_16x16x64_i8 v[118:121], v[146:149], v[162:165], v[118:121]
	v_mfma_i32_16x16x64_i8 v[114:117], v[154:157], v[162:165], v[114:117]
	v_mfma_i32_16x16x64_i8 v[102:105], v[146:149], v[182:185], v[102:105]
	v_mfma_i32_16x16x64_i8 v[98:101], v[154:157], v[182:185], v[98:101]
	v_mfma_i32_16x16x64_i8 v[86:89], v[146:149], v[190:193], v[86:89]
	v_mfma_i32_16x16x64_i8 v[82:85], v[154:157], v[190:193], v[82:85]
	v_mfma_i32_16x16x64_i8 v[70:73], v[146:149], v[208:211], v[70:73]
	v_mfma_i32_16x16x64_i8 v[66:69], v[154:157], v[208:211], v[66:69]
	v_mfma_i32_16x16x64_i8 v[118:121], v[150:153], v[166:169], v[118:121]
	v_mfma_i32_16x16x64_i8 v[114:117], v[158:161], v[166:169], v[114:117]
	v_mfma_i32_16x16x64_i8 v[102:105], v[150:153], v[186:189], v[102:105]
	v_mfma_i32_16x16x64_i8 v[98:101], v[158:161], v[186:189], v[98:101]
	v_mfma_i32_16x16x64_i8 v[86:89], v[150:153], v[194:197], v[86:89]
	v_mfma_i32_16x16x64_i8 v[82:85], v[158:161], v[194:197], v[82:85]
	v_mfma_i32_16x16x64_i8 v[70:73], v[150:153], v[212:215], v[70:73]
	v_mfma_i32_16x16x64_i8 v[66:69], v[158:161], v[212:215], v[66:69]
	s_setprio 0
	s_barrier
	s_mov_b32 s55, s85
	ds_read_b128 v[162:165], v177 offset:16384
	ds_read_b128 v[166:169], v177 offset:17408
	ds_read_b128 v[182:185], v177 offset:18432
	ds_read_b128 v[186:189], v177 offset:19456
	ds_read_b128 v[190:193], v177 offset:20480
	ds_read_b128 v[194:197], v177 offset:21504
	ds_read_b128 v[208:211], v177 offset:22528
	ds_read_b128 v[212:215], v177 offset:23552
	s_add_i32 m0, s55, 0x10000
	s_mov_b32 s55, s85
	buffer_load_dwordx4 v172, s[64:67], s51 offen lds
	s_add_i32 m0, s55, 0x12000
	s_mov_b32 s58, s85
	buffer_load_dwordx4 v174, s[64:67], s51 offen lds
	s_add_i32 s55, s51, 0x4000
	s_add_i32 m0, s58, 0x14000
	s_mov_b32 s58, s85
	buffer_load_dwordx4 v172, s[64:67], s55 offen lds
	s_add_i32 m0, s58, 0x16000
	s_nop 0
	buffer_load_dwordx4 v174, s[64:67], s55 offen lds
	s_mov_b32 s55, s85
	s_mov_b32 m0, s55
	s_mov_b32 s55, s85
	buffer_load_dwordx4 v0, s[88:91], s54 offen lds
	s_add_i32 m0, s55, 0x2000
	s_nop 0
	buffer_load_dwordx4 v173, s[88:91], s54 offen lds
	s_cmp_lg_u32 s53, 0
	s_cbranch_scc1 .Lgr1
	s_waitcnt vmcnt(8)

; #define PG8_STAGE(bufoff, RS, soff, voff) do { _Pragma("unroll") for (int _i = 0; _i < 2; ++_i) \
;         __builtin_amdgcn_raw_ptr_buffer_load_lds(RS, (PG8_LAS void*)(lds + (bufoff) + sgpr_opaque(ldsw) + _i * 8192), 16, (int)(voff)[_i], (int)(soff), 0, 0); } while (0)
; #define PG8_LDA(dst, b, h) do { _Pragma("unroll") for (int m = 0; m < 4; ++m) _Pragma("unroll") for (int k = 0; k < 2; ++k) dst[m][k] = *(const PG8_LAS f16x8*)(lds + PG8_SA(b, h) + aoff + m * 2048 + k * 1024); } while (0)
; #define PG8_LDB(dst, b, h) do { _Pragma("unroll") for (int n = 0; n < 2; ++n) _Pragma("unroll") for (int k = 0; k < 2; ++k) dst[n][k] = *(const PG8_LAS f16x8*)(lds + PG8_SB(b, h) + boff + n * 2048 + k * 1024); } while (0)
; #define PG8_WAIT_L(n) asm volatile("s_waitcnt lgkmcnt(" #n ")" ::: "memory")
; #define PG8_BAR __builtin_amdgcn_s_barrier()
; #define PG8_SCHED __builtin_amdgcn_sched_barrier(0)
; template <class Epi, class Sched, bool ALIGN_EPI = false, bool SP2 = false, bool I8 = false, bool ATILED = false>
; __device__ __forceinline__ void gemm_phase(PG8_LAS unsigned char* lds, const Gemm g, const Sched& S, const Epi& E, const int wid) {
;     ...
;             PG8_WAIT_VG; PG8_WAIT_L(0); PG8_BAR; PG8_MMA(1, 0, At, B0); PG8_MMA(1, 1, At, B1); PG8_BAR; PG8_SCHED;
;             PG8_LDB(B0, 1, 0); PG8_LDB(B1, 1, 1); PG8_SCHED; PG8_LDA(At, 1, 0); PG8_STAGE(PG8_SA(0, 1), rsA, a2 + hstepA, voffA);
;             PG8_WAIT_VG; PG8_WAIT_L(0); PG8_BAR; PG8_MMA(0, 0, At, B0); PG8_MMA(0, 1, At, B1); PG8_BAR; PG8_SCHED;
;             PG8_LDA(At, 1, 1); PG8_STAGE(PG8_SB(1, 0), rsB, b3, voffB); PG8_STAGE(PG8_SB(1, 1), rsB, b3 + hstep, voffB); PG8_STAGE(PG8_SA(1, 0), rsA, a3, voffA);
;             PG8_WAIT_VG; PG8_WAIT_L(0); PG8_BAR; PG8_MMA(1, 0, At, B0); PG8_MMA(1, 1, At, B1); PG8_BAR; PG8_SCHED;
.Lgr2:
	s_waitcnt vmcnt(24)
	s_waitcnt lgkmcnt(0)
	s_barrier
	s_setprio 1
	s_waitcnt lgkmcnt(7)
	v_mfma_i32_16x16x64_i8 v[126:129], v[130:133], v[162:165], v[126:129]
	v_mfma_i32_16x16x64_i8 v[122:125], v[138:141], v[162:165], v[122:125]
	s_waitcnt lgkmcnt(5)
	v_mfma_i32_16x16x64_i8 v[110:113], v[130:133], v[182:185], v[110:113]
	v_mfma_i32_16x16x64_i8 v[106:109], v[138:141], v[182:185], v[106:109]
	s_waitcnt lgkmcnt(3)
	v_mfma_i32_16x16x64_i8 v[94:97], v[130:133], v[190:193], v[94:97]
	v_mfma_i32_16x16x64_i8 v[90:93], v[138:141], v[190:193], v[90:93]
	s_waitcnt lgkmcnt(1)
	v_mfma_i32_16x16x64_i8 v[78:81], v[130:133], v[208:211], v[78:81]
	v_mfma_i32_16x16x64_i8 v[74:77], v[138:141], v[208:211], v[74:77]
	v_mfma_i32_16x16x64_i8 v[126:129], v[134:137], v[166:169], v[126:129]
	v_mfma_i32_16x16x64_i8 v[122:125], v[142:145], v[166:169], v[122:125]
	v_mfma_i32_16x16x64_i8 v[110:113], v[134:137], v[186:189], v[110:113]
	v_mfma_i32_16x16x64_i8 v[106:109], v[142:145], v[186:189], v[106:109]
	v_mfma_i32_16x16x64_i8 v[94:97], v[134:137], v[194:197], v[94:97]
	v_mfma_i32_16x16x64_i8 v[90:93], v[142:145], v[194:197], v[90:93]
	s_waitcnt lgkmcnt(0)
	v_mfma_i32_16x16x64_i8 v[78:81], v[134:137], v[212:215], v[78:81]
	v_mfma_i32_16x16x64_i8 v[74:77], v[142:145], v[212:215], v[74:77]
	s_setprio 0
	s_setprio 1
	v_mfma_i32_16x16x64_i8 v[118:121], v[146:149], v[162:165], v[118:121]
	v_mfma_i32_16x16x64_i8 v[114:117], v[154:157], v[162:165], v[114:117]
	v_mfma_i32_16x16x64_i8 v[102:105], v[146:149], v[182:185], v[102:105]
	v_mfma_i32_16x16x64_i8 v[98:101], v[154:157], v[182:185], v[98:101]
	v_mfma_i32_16x16x64_i8 v[86:89], v[146:149], v[190:193], v[86:89]
	v_mfma_i32_16x16x64_i8 v[82:85], v[154:157], v[190:193], v[82:85]
	v_mfma_i32_16x16x64_i8 v[70:73], v[146:149], v[208:211], v[70:73]
	v_mfma_i32_16x16x64_i8 v[66:69], v[154:157], v[208:211], v[66:69]
	v_mfma_i32_16x16x64_i8 v[118:121], v[150:153], v[166:169], v[118:121]
	v_mfma_i32_16x16x64_i8 v[114:117], v[158:161], v[166:169], v[114:117]
	v_mfma_i32_16x16x64_i8 v[102:105], v[150:153], v[186:189], v[102:105]
	v_mfma_i32_16x16x64_i8 v[98:101], v[158:161], v[186:189], v[98:101]
	v_mfma_i32_16x16x64_i8 v[86:89], v[150:153], v[194:197], v[86:89]
	v_mfma_i32_16x16x64_i8 v[82:85], v[158:161], v[194:197], v[82:85]
	v_mfma_i32_16x16x64_i8 v[70:73], v[150:153], v[212:215], v[70:73]
	v_mfma_i32_16x16x64_i8 v[66:69], v[158:161], v[212:215], v[66:69]
	s_setprio 0
	s_barrier
	s_mov_b32 s54, s85
	ds_read_b128 v[162:165], v177 offset:49152
	ds_read_b128 v[166:169], v177 offset:50176
	ds_read_b128 v[182:185], v177 offset:51200
	ds_read_b128 v[186:189], v177 offset:52224
	ds_read_b128 v[190:193], v177 offset:53248
	ds_read_b128 v[194:197], v177 offset:54272
	ds_read_b128 v[208:211], v177 offset:55296
	ds_read_b128 v[212:215], v177 offset:56320
	s_add_i32 m0, s54, 0x18000
	s_mov_b32 s54, s85
	buffer_load_dwordx4 v172, s[64:67], s52 offen lds
	s_add_i32 m0, s54, 0x1a000
	s_add_i32 s51, s51, 0xc000
	buffer_load_dwordx4 v174, s[64:67], s52 offen lds
	s_mov_b32 s52, s85
	s_add_i32 m0, s52, 0x1c000
	s_mov_b32 s52, s85
	buffer_load_dwordx4 v172, s[64:67], s51 offen lds
	s_add_i32 m0, s52, 0x1e000
	s_nop 0
	buffer_load_dwordx4 v174, s[64:67], s51 offen lds
	s_mov_b32 s51, s85
	s_add_i32 m0, s51, 0x8000
	s_mov_b32 s51, s85
	buffer_load_dwordx4 v0, s[88:91], s50 offen lds
	s_add_i32 m0, s51, 0xa000
	s_nop 0
	buffer_load_dwordx4 v173, s[88:91], s50 offen lds
	s_cmp_lg_u32 s53, 0
	s_cbranch_scc1 .Lgr3
	s_waitcnt vmcnt(8)
.Lgr3:
	s_waitcnt vmcnt(24)
	s_waitcnt lgkmcnt(0)
	s_barrier
	s_setprio 1
	s_waitcnt lgkmcnt(7)
	v_mfma_i32_16x16x64_i8 v[62:65], v[130:133], v[162:165], v[62:65]
	v_mfma_i32_16x16x64_i8 v[58:61], v[138:141], v[162:165], v[58:61]
	s_waitcnt lgkmcnt(5)
	v_mfma_i32_16x16x64_i8 v[46:49], v[130:133], v[182:185], v[46:49]
	v_mfma_i32_16x16x64_i8 v[42:45], v[138:141], v[182:185], v[42:45]
	s_waitcnt lgkmcnt(3)
	v_mfma_i32_16x16x64_i8 v[30:33], v[130:133], v[190:193], v[30:33]
	v_mfma_i32_16x16x64_i8 v[26:29], v[138:141], v[190:193], v[26:29]
	s_waitcnt lgkmcnt(1)
	v_mfma_i32_16x16x64_i8 v[14:17], v[130:133], v[208:211], v[14:17]
	v_mfma_i32_16x16x64_i8 v[10:13], v[138:141], v[208:211], v[10:13]
	v_mfma_i32_16x16x64_i8 v[62:65], v[134:137], v[166:169], v[62:65]
	v_mfma_i32_16x16x64_i8 v[58:61], v[142:145], v[166:169], v[58:61]
	v_mfma_i32_16x16x64_i8 v[46:49], v[134:137], v[186:189], v[46:49]
	v_mfma_i32_16x16x64_i8 v[42:45], v[142:145], v[186:189], v[42:45]
	v_mfma_i32_16x16x64_i8 v[30:33], v[134:137], v[194:197], v[30:33]
	v_mfma_i32_16x16x64_i8 v[26:29], v[142:145], v[194:197], v[26:29]
	s_waitcnt lgkmcnt(0)
	v_mfma_i32_16x16x64_i8 v[14:17], v[134:137], v[212:215], v[14:17]
	v_mfma_i32_16x16x64_i8 v[10:13], v[142:145], v[212:215], v[10:13]
	s_setprio 0
	s_setprio 1
	v_mfma_i32_16x16x64_i8 v[54:57], v[146:149], v[162:165], v[54:57]
	v_mfma_i32_16x16x64_i8 v[50:53], v[154:157], v[162:165], v[50:53]
	v_mfma_i32_16x16x64_i8 v[38:41], v[146:149], v[182:185], v[38:41]
	v_mfma_i32_16x16x64_i8 v[34:37], v[154:157], v[182:185], v[34:37]
	v_mfma_i32_16x16x64_i8 v[22:25], v[146:149], v[190:193], v[22:25]
	v_mfma_i32_16x16x64_i8 v[18:21], v[154:157], v[190:193], v[18:21]
	v_mfma_i32_16x16x64_i8 v[6:9], v[146:149], v[208:211], v[6:9]
	v_mfma_i32_16x16x64_i8 v[2:5], v[154:157], v[208:211], v[2:5]
	v_mfma_i32_16x16x64_i8 v[54:57], v[150:153], v[166:169], v[54:57]
	v_mfma_i32_16x16x64_i8 v[50:53], v[158:161], v[166:169], v[50:53]
	v_mfma_i32_16x16x64_i8 v[38:41], v[150:153], v[186:189], v[38:41]
	v_mfma_i32_16x16x64_i8 v[34:37], v[158:161], v[186:189], v[34:37]
	v_mfma_i32_16x16x64_i8 v[22:25], v[150:153], v[194:197], v[22:25]
	v_mfma_i32_16x16x64_i8 v[18:21], v[158:161], v[194:197], v[18:21]
	v_mfma_i32_16x16x64_i8 v[6:9], v[150:153], v[212:215], v[6:9]
	v_mfma_i32_16x16x64_i8 v[2:5], v[158:161], v[212:215], v[2:5]
	s_setprio 0
	s_barrier
	s_add_i32 s49, s49, 2
	s_addk_i32 s47, 0x100
	s_add_i32 s48, s48, 0x10000
	s_cmp_gt_u32 s49, 5
	s_cbranch_scc0 .LBB0_483
	s_and_b64 vcc, exec, s[56:57]
	s_cbranch_vccz .LBB0_486
	s_barrier

;     __host__ __device__ bool next(int i, Unit& u) const { if (!so.next(i / 3, u)) return false; u.pn += 4 * (i % 3); u.idx = i; return true; }
; #define PG8_BAR __builtin_amdgcn_s_barrier()
; template <class Epi, class Sched, bool ALIGN_EPI = false, bool SP2 = false, bool I8 = false, bool ATILED = false>
; __device__ __forceinline__ void gemm_phase(PG8_LAS unsigned char* lds, const Gemm g, const Sched& S, const Epi& E, const int wid) {
;     ...
;     for (int i = 0; i < 2; ++i) { int R, C; stage_rc(tid * 16 + i * 8192, R, C); const int Rb = Epi::PERM ? ((R & ~31) + perm32(R & 31)) : R;
;         voffA[i] = (unsigned)(R * (ATILED ? BK : K) + C) * 2u; voffB[i] = (unsigned)(Rb * K + C) * 2u; }
;     const unsigned kstep = (unsigned)(BK * 2);
;     const unsigned hstep = (unsigned)HALF * K * 2;
;     const unsigned tstep = 2 * hstep;
;     const unsigned kstepA = ATILED ? (unsigned)(BM * BK * 2) : kstep, hstepA = ATILED ? (unsigned)(HALF * BK * 2) : hstep, tstepA = ATILED ? (unsigned)nt * (unsigned)(BM * BK * 2) : tstep;
;     const __amdgpu_buffer_rsrc_t rsA = __builtin_amdgcn_make_buffer_rsrc((void*)g.A, 0, 0x7fffffff, 0x00020000), rsB = __builtin_amdgcn_make_buffer_rsrc((void*)g.Bt, 0, 0x7fffffff, 0x00020000);
;     const unsigned ldsw = (unsigned)wid * 1024u;
;     const int aoff = lds_byte(wr * 64 + fr, fq * 8), boff = lds_byte(wc * 32 + fr, fq * 8);
;     ...
;     Unit cur, nxt; int ui = 0;
;     if (!S.next(0, cur)) return;
;     f32x4 acc[2][2][4][2];
; #pragma unroll
;     for (int a = 0; a < 2; ++a)
; #pragma unroll
;         for (int b = 0; b < 2; ++b)
; #pragma unroll
;             for (int m = 0; m < 4; ++m)
; #pragma unroll
;                 for (int n = 0; n < 2; ++n) acc[a][b][m][n] = (f32x4){0.f, 0.f, 0.f, 0.f};
;     f16x8 At[4][2], B0[2][2], B1[2][2];
;     unsigned cA = (unsigned)cur.pm * tstepA + (unsigned)(cur.pm >> 4) * g.gapA, cB = (unsigned)cur.pn * tstep;
;     S.a_ready(cur);
;     if constexpr (SP2) {
;         PG8_STAGE(PG8_SB(0, 0), rsB, cB, voffB); PG8_STAGE(PG8_SB(0, 1), rsB, cB + hstep, voffB); PG8_STAGE(PG8_SA(0, 0), rsA, cA, voffA); PG8_STAGE(PG8_SA(0, 1), rsA, cA + hstepA, voffA);
;         if (wr == 1) PG8_BAR;
;         PG8_WAIT_V(2); PG8_BAR;
;         PG8_STAGE(PG8_SB(1, 0), rsB, cB + kstep, voffB); PG8_STAGE(PG8_SA(1, 0), rsA, cA + kstepA, voffA); PG8_STAGE(PG8_SB(1, 1), rsB, cB + hstep + kstep, voffB);
;         PG8_WAIT_V(6); PG8_BAR;
.LBB0_1210:
	s_and_b64 vcc, exec, s[30:31]
	s_waitcnt lgkmcnt(0)
	s_barrier
	v_mbcnt_lo_u32_b32 v2, -1, 0
	v_mbcnt_hi_u32_b32 v2, -1, v2
	s_cbranch_vccnz .LBB0_1297
	v_lshl_add_u32 v3, v2, 4, s85
	v_ashrrev_i32_e32 v0, 31, v3
	v_lshrrev_b32_e32 v0, 22, v0
	v_add_u32_e32 v0, v3, v0
	v_ashrrev_i32_e32 v0, 10, v0
	s_waitcnt vmcnt(0)
	v_mul_i32_i24_e32 v4, 0x400, v0
	v_sub_u32_e32 v4, v3, v4
	v_lshrrev_b32_e32 v5, 4, v4
	v_bitop3_b32 v4, v5, v4, 32 bitop3:0x6c
	v_ashrrev_i32_e32 v6, 31, v4
	s_mul_hi_i32 s27, s26, 0x300000
	s_mul_i32 s26, s26, 0x300000
	v_lshrrev_b32_e32 v6, 26, v6
	s_add_u32 s26, s48, s26
	v_lshlrev_b32_e32 v5, 3, v0
	v_add_u32_e32 v6, v4, v6
	s_addc_u32 s27, s49, s27
	v_and_b32_e32 v5, -16, v5
	v_ashrrev_i32_e32 v7, 6, v6
	v_and_b32_e32 v6, 0xc0, v6
	s_add_u32 s64, s26, 0x1ea00000
	v_add_u32_e32 v5, v7, v5
	v_sub_u32_e32 v4, v4, v6
	s_addc_u32 s26, s27, 0
	v_lshlrev_b32_e32 v0, 5, v0
	v_ashrrev_i16_sdwa v4, v232, sext(v4) dst_sel:DWORD dst_unused:UNUSED_PAD src0_sel:DWORD src1_sel:BYTE_0
	v_lshlrev_b32_e32 v6, 1, v5
	v_lshrrev_b32_e32 v8, 2, v5
	v_and_b32_e32 v7, 3, v7
	s_mov_b32 s27, 0x3fffe0
	v_and_b32_e32 v0, 32, v0
	v_bfe_i32 v4, v4, 0, 16
	v_and_b32_e32 v6, 24, v6
	v_and_b32_e32 v8, 4, v8
	v_and_or_b32 v7, v5, s27, v7
	v_or3_b32 v6, v7, v8, v6
	v_add_lshl_u32 v4, v0, v4, 1
	v_add_u32_e32 v3, 0x2000, v3
	v_lshl_add_u32 v0, v5, 10, v4
	v_mbcnt_lo_u32_b32 v194, -1, 0
	v_mbcnt_hi_u32_b32 v194, -1, v194
	v_lshl_add_u32 v194, v194, 4, s85
	v_ashrrev_i32_e32 v4, 31, v3
	v_lshrrev_b32_e32 v4, 22, v4
	v_add_u32_e32 v4, v3, v4
	v_ashrrev_i32_e32 v4, 10, v4
	v_mul_i32_i24_e32 v5, 0x400, v4
	v_sub_u32_e32 v3, v3, v5
	v_lshrrev_b32_e32 v5, 4, v3
	v_bitop3_b32 v3, v5, v3, 32 bitop3:0x6c
	v_ashrrev_i32_e32 v6, 31, v3
	v_lshrrev_b32_e32 v6, 26, v6
	v_add_u32_e32 v6, v3, v6
	v_ashrrev_i32_e32 v7, 6, v6
	v_and_b32_e32 v6, 0xffc0, v6
	v_sub_u32_e32 v3, v3, v6
	v_lshlrev_b32_e32 v5, 3, v4
	v_lshrrev_b16_e32 v6, 7, v3
	v_and_b32_e32 v5, -16, v5
	v_and_b32_e32 v6, 1, v6
	v_add_u32_e32 v5, v7, v5
	v_add_u16_e32 v3, v3, v6
	s_and_b32 s65, s26, 0xffff
	s_mov_b32 s26, s85
	v_lshlrev_b32_e32 v4, 5, v4
	v_ashrrev_i16_sdwa v3, v232, sext(v3) dst_sel:DWORD dst_unused:UNUSED_PAD src0_sel:DWORD src1_sel:BYTE_0
	v_lshlrev_b32_e32 v6, 1, v5
	v_lshrrev_b32_e32 v8, 2, v5
	v_and_b32_e32 v7, 3, v7
	v_and_b32_e32 v4, 32, v4
	v_bfe_i32 v3, v3, 0, 16
	v_and_b32_e32 v6, 24, v6
	v_and_b32_e32 v8, 4, v8
	v_and_or_b32 v7, v5, s27, v7
	s_add_i32 m0, s26, 0x10000
	v_readlane_b32 s27, v255, 3
	s_bfe_u32 s100, s27, 0x10011
	s_bfe_u32 s101, s27, 0x10007
	s_and_b32 s27, s27, 0xfffc0000
	s_lshl_b32 s100, s100, 14
	s_lshl_b32 s101, s101, 15
	s_or_b32 s27, s27, s100
	s_or_b32 s27, s27, s101
	s_mov_b32 s26, s85
	v_or3_b32 v6, v7, v8, v6
	v_add_lshl_u32 v3, v4, v3, 1
	v_mbcnt_lo_u32_b32 v196, -1, 0
	v_mbcnt_hi_u32_b32 v196, -1, v196
	v_lshl_add_u32 v196, v196, 4, s85
	v_add_u32_e32 v196, 0x2000, v196
	s_mov_b32 s90, s66
	buffer_load_dwordx4 v194, s[64:67], s27 offen lds
	s_add_i32 m0, s26, 0x12000
	s_mov_b32 s26, s85
	buffer_load_dwordx4 v196, s[64:67], s27 offen lds
	s_add_i32 m0, s26, 0x14000
	v_readlane_b32 s27, v254, 61
	s_bfe_u32 s100, s27, 0x10011
	s_bfe_u32 s101, s27, 0x10007
	s_and_b32 s27, s27, 0xfffc0000
	s_lshl_b32 s100, s100, 14
	s_lshl_b32 s101, s101, 15
	s_or_b32 s27, s27, s100
	s_or_b32 s27, s27, s101
	s_mov_b32 s26, s85
	s_mov_b32 s91, s67
	v_lshl_add_u32 v195, v5, 10, v3
	v_readlane_b32 s22, v253, 31
	v_readlane_b32 s23, v253, 32
	buffer_load_dwordx4 v194, s[64:67], s27 offen lds
	s_add_i32 m0, s26, 0x16000
	s_mov_b32 s26, s85
	buffer_load_dwordx4 v196, s[64:67], s27 offen lds
	s_mov_b32 m0, s26
	v_readlane_b32 s27, v255, 1
	s_mov_b32 s26, s85
	s_and_b64 vcc, exec, s[22:23]
	s_nop 2
	buffer_load_dwordx4 v0, s[88:91], s27 offen lds
	s_add_i32 m0, s26, 0x2000
	s_mov_b32 s26, s85
	buffer_load_dwordx4 v195, s[88:91], s27 offen lds
	s_add_i32 m0, s26, 0x4000
	v_readlane_b32 s27, v254, 63
	s_mov_b32 s26, s85
	s_nop 3
	buffer_load_dwordx4 v0, s[88:91], s27 offen lds
	s_add_i32 m0, s26, 0x6000
	s_nop 0
	buffer_load_dwordx4 v195, s[88:91], s27 offen lds
	s_cbranch_vccnz .LBB0_1213
	s_barrier
.LBB0_1213:
	s_add_u32 s40, s44, 0xe800000
	s_addc_u32 s41, s45, 0
	s_mov_b32 s26, s85
	s_add_u32 s42, s46, 0x10000000
	s_waitcnt vmcnt(2)
	s_barrier
	s_addc_u32 s43, s47, 0
	s_add_i32 m0, s26, 0x18000
	v_readlane_b32 s27, v255, 0
	s_bfe_u32 s100, s27, 0x10011
	s_bfe_u32 s101, s27, 0x10007
	s_and_b32 s27, s27, 0xfffc0000
	s_lshl_b32 s100, s100, 14
	s_lshl_b32 s101, s101, 15
	s_or_b32 s27, s27, s100
	s_or_b32 s27, s27, s101
	s_mov_b32 s26, s85
	v_and_b32_e32 v197, 15, v2
	v_or_b32_e32 v208, s96, v197
	v_lshlrev_b32_e32 v5, 6, v208
	v_and_b32_e32 v6, 48, v2
	buffer_load_dwordx4 v194, s[64:67], s27 offen lds
	s_add_i32 m0, s26, 0x1a000
	s_mov_b32 s26, s85
	buffer_load_dwordx4 v196, s[64:67], s27 offen lds
	s_add_i32 m0, s26, 0x8000
	v_readlane_b32 s27, v255, 2
	s_mov_b32 s26, s85
	v_ashrrev_i32_e32 v4, 6, v2
	v_ashrrev_i32_e32 v3, 1, v2
	v_lshlrev_b32_e32 v8, 2, v208
	v_and_b32_e32 v3, -8, v3
	buffer_load_dwordx4 v0, s[88:91], s27 offen lds
	s_add_i32 m0, s26, 0xa000
	s_mov_b32 s26, s85
	buffer_load_dwordx4 v195, s[88:91], s27 offen lds
	s_add_i32 m0, s26, 0x1c000
	v_readlane_b32 s27, v255, 4
	s_bfe_u32 s100, s27, 0x10011
	s_bfe_u32 s101, s27, 0x10007
	s_and_b32 s27, s27, 0xfffc0000
	s_lshl_b32 s100, s100, 14
	s_lshl_b32 s101, s101, 15
	s_or_b32 s27, s27, s100
	s_or_b32 s27, s27, s101
	s_mov_b32 s26, s85
	v_and_b32_e32 v8, 32, v8
	v_lshlrev_b32_e32 v2, 2, v2
	v_and_b32_e32 v2, 32, v2
	s_mov_b32 s46, 0
	buffer_load_dwordx4 v194, s[64:67], s27 offen lds
	s_add_i32 m0, s26, 0x1e000
	s_movk_i32 s26, 0x3c0
	buffer_load_dwordx4 v196, s[64:67], s27 offen lds
	v_and_or_b32 v5, v5, s26, v6
	v_readlane_b32 s26, v253, 60
	s_waitcnt vmcnt(6)
	s_add_u32 s44, s44, 0xf000000
	s_addc_u32 s45, s45, 0
	v_lshl_add_u32 v7, v4, 10, s26
	v_readlane_b32 s26, v253, 62
	v_bitop3_b32 v209, v5, v7, v8 bitop3:0xde
	v_lshl_or_b32 v5, v197, 6, v6
	v_add_lshl_u32 v4, v4, s26, 10
	v_readlane_b32 s26, v253, 61
	v_bitop3_b32 v210, v5, v4, v2 bitop3:0xde
	v_readlane_b32 s47, v254, 60
	v_add_u32_e32 v237, s26, v3
	v_lshlrev_b32_e32 v2, 2, v237
	v_add_u32_e32 v199, 0x22400, v2
	v_add_u32_e32 v244, 0x24400, v2
	v_readlane_b32 s26, v254, 62
	v_readlane_b32 s49, v255, 3
	v_readlane_b32 s48, v255, 1
	s_mov_b32 s50, 0
	s_barrier
	s_branch .LBB0_1216

;     __host__ __device__ bool next(int i, Unit& u) const { if (!so.next(i / 3, u)) return false; u.pn += 4 * (i % 3); u.idx = i; return true; }
; #define PG8_STAGE(bufoff, RS, soff, voff) do { _Pragma("unroll") for (int _i = 0; _i < 2; ++_i) \
;         __builtin_amdgcn_raw_ptr_buffer_load_lds(RS, (PG8_LAS void*)(lds + (bufoff) + sgpr_opaque(ldsw) + _i * 8192), 16, (int)(voff)[_i], (int)(soff), 0, 0); } while (0)
; #define PG8_LDA(dst, b, h) do { _Pragma("unroll") for (int m = 0; m < 4; ++m) _Pragma("unroll") for (int k = 0; k < 2; ++k) dst[m][k] = *(const PG8_LAS f16x8*)(lds + PG8_SA(b, h) + aoff + m * 2048 + k * 1024); } while (0)
; #define PG8_LDB(dst, b, h) do { _Pragma("unroll") for (int n = 0; n < 2; ++n) _Pragma("unroll") for (int k = 0; k < 2; ++k) dst[n][k] = *(const PG8_LAS f16x8*)(lds + PG8_SB(b, h) + boff + n * 2048 + k * 1024); } while (0)
; template <class Epi, class Sched, bool ALIGN_EPI = false, bool SP2 = false, bool I8 = false, bool ATILED = false>
; __device__ __forceinline__ void gemm_phase(PG8_LAS unsigned char* lds, const Gemm g, const Sched& S, const Epi& E, const int wid) {
;     ...
;         const bool has_next = S.next(ui + 1, nxt);
;         const unsigned nA = has_next ? (unsigned)nxt.pm * tstepA + (unsigned)(nxt.pm >> 4) * g.gapA : cA, nB = has_next ? (unsigned)nxt.pn * tstep : cB;
;         for (int t = 0; t < nt; t += 2) {
;             const bool last = (t == nt - 2);
;             const unsigned a1 = cA + (unsigned)(t + 1) * kstepA;
;             const unsigned a2 = last ? nA : cA + (unsigned)(t + 2) * kstepA, b2 = last ? nB : cB + (unsigned)(t + 2) * kstep;
;             const unsigned a3 = a2 + kstepA, b3 = b2 + kstep;
;             if (last && has_next) S.a_ready(nxt);
;             if constexpr (SP2) {
;             const int grace = __builtin_amdgcn_readfirstlane((PG8_GRACE && Epi::NSTORE > 0 && t == 0 && ui > 0) ? 1 : 0);
;     ...
;             PG8_LDB(B0, 0, 0); PG8_LDB(B1, 0, 1); PG8_SCHED; PG8_LDA(At, 0, 0); PG8_STAGE(PG8_SA(1, 1), rsA, a1 + hstepA, voffA);
;     ...
; #pragma unroll
;         for (int a = 0; a < 2; ++a)
; #pragma unroll
;             for (int b = 0; b < 2; ++b)
; #pragma unroll
;                 for (int m = 0; m < 4; ++m)
; #pragma unroll
;                     for (int n = 0; n < 2; ++n) acc[a][b][m][n] = (f32x4){0.f, 0.f, 0.f, 0.f};
;         cur = nxt; cA = nA; cB = nB; ++ui;
.LBB0_1222:
	s_lshl_b32 s59, s54, 18
	s_and_b64 s[36:37], s[34:35], exec
	s_cselect_b32 s38, s59, s48
	s_lshl_b32 s60, s55, 18
	s_and_b64 s[36:37], s[34:35], exec
	s_cselect_b32 s39, s60, s49
	s_cmp_lg_u32 s50, 0
	v_mov_b32_e32 v2, 0
	s_cselect_b64 s[36:37], -1, 0
	s_add_i32 s48, s48, 0x20080
	s_add_i32 s49, s49, 0x10000
	s_mov_b32 s50, -2
	v_mov_b32_e32 v3, v2
	v_mov_b32_e32 v4, v2
	v_mov_b32_e32 v5, v2
	v_mov_b32_e32 v6, v2
	v_mov_b32_e32 v7, v2
	v_mov_b32_e32 v8, v2
	v_mov_b32_e32 v9, v2
	v_mov_b32_e32 v18, v2
	v_mov_b32_e32 v19, v2
	v_mov_b32_e32 v20, v2
	v_mov_b32_e32 v21, v2
	v_mov_b32_e32 v22, v2
	v_mov_b32_e32 v23, v2
	v_mov_b32_e32 v24, v2
	v_mov_b32_e32 v25, v2
	v_mov_b32_e32 v82, v2
	v_mov_b32_e32 v83, v2
	v_mov_b32_e32 v84, v2
	v_mov_b32_e32 v85, v2
	v_mov_b32_e32 v86, v2
	v_mov_b32_e32 v87, v2
	v_mov_b32_e32 v88, v2
	v_mov_b32_e32 v89, v2
	v_mov_b32_e32 v98, v2
	v_mov_b32_e32 v99, v2
	v_mov_b32_e32 v100, v2
	v_mov_b32_e32 v101, v2
	v_mov_b32_e32 v102, v2
	v_mov_b32_e32 v103, v2
	v_mov_b32_e32 v104, v2
	v_mov_b32_e32 v105, v2
	v_mov_b32_e32 v10, v2
	v_mov_b32_e32 v11, v2
	v_mov_b32_e32 v12, v2
	v_mov_b32_e32 v13, v2
	v_mov_b32_e32 v14, v2
	v_mov_b32_e32 v15, v2
	v_mov_b32_e32 v16, v2
	v_mov_b32_e32 v17, v2
	v_mov_b32_e32 v74, v2
	v_mov_b32_e32 v75, v2
	v_mov_b32_e32 v76, v2
	v_mov_b32_e32 v77, v2
	v_mov_b32_e32 v78, v2
	v_mov_b32_e32 v79, v2
	v_mov_b32_e32 v80, v2
	v_mov_b32_e32 v81, v2
	v_mov_b32_e32 v90, v2
	v_mov_b32_e32 v91, v2
	v_mov_b32_e32 v92, v2
	v_mov_b32_e32 v93, v2
	v_mov_b32_e32 v94, v2
	v_mov_b32_e32 v95, v2
	v_mov_b32_e32 v96, v2
	v_mov_b32_e32 v97, v2
	v_mov_b32_e32 v106, v2
	v_mov_b32_e32 v107, v2
	v_mov_b32_e32 v108, v2
	v_mov_b32_e32 v109, v2
	v_mov_b32_e32 v110, v2
	v_mov_b32_e32 v111, v2
	v_mov_b32_e32 v112, v2
	v_mov_b32_e32 v113, v2
	v_mov_b32_e32 v114, v2
	v_mov_b32_e32 v115, v2
	v_mov_b32_e32 v116, v2
	v_mov_b32_e32 v117, v2
	v_mov_b32_e32 v118, v2
	v_mov_b32_e32 v119, v2
	v_mov_b32_e32 v120, v2
	v_mov_b32_e32 v121, v2
	v_mov_b32_e32 v130, v2
	v_mov_b32_e32 v131, v2
	v_mov_b32_e32 v132, v2
	v_mov_b32_e32 v133, v2
	v_mov_b32_e32 v134, v2
	v_mov_b32_e32 v135, v2
	v_mov_b32_e32 v136, v2
	v_mov_b32_e32 v137, v2
	v_mov_b32_e32 v146, v2
	v_mov_b32_e32 v147, v2
	v_mov_b32_e32 v148, v2
	v_mov_b32_e32 v149, v2
	v_mov_b32_e32 v150, v2
	v_mov_b32_e32 v151, v2
	v_mov_b32_e32 v152, v2
	v_mov_b32_e32 v153, v2
	v_mov_b32_e32 v166, v2
	v_mov_b32_e32 v167, v2
	v_mov_b32_e32 v168, v2
	v_mov_b32_e32 v169, v2
	v_mov_b32_e32 v170, v2
	v_mov_b32_e32 v171, v2
	v_mov_b32_e32 v172, v2
	v_mov_b32_e32 v173, v2
	v_mov_b32_e32 v122, v2
	v_mov_b32_e32 v123, v2
	v_mov_b32_e32 v124, v2
	v_mov_b32_e32 v125, v2
	v_mov_b32_e32 v126, v2
	v_mov_b32_e32 v127, v2
	v_mov_b32_e32 v128, v2
	v_mov_b32_e32 v129, v2
	v_mov_b32_e32 v138, v2
	v_mov_b32_e32 v139, v2
	v_mov_b32_e32 v140, v2
	v_mov_b32_e32 v141, v2
	v_mov_b32_e32 v142, v2
	v_mov_b32_e32 v143, v2
	v_mov_b32_e32 v144, v2
	v_mov_b32_e32 v145, v2
	v_mov_b32_e32 v154, v2
	v_mov_b32_e32 v155, v2
	v_mov_b32_e32 v156, v2
	v_mov_b32_e32 v157, v2
	v_mov_b32_e32 v158, v2
	v_mov_b32_e32 v159, v2
	v_mov_b32_e32 v160, v2
	v_mov_b32_e32 v161, v2
	v_mov_b32_e32 v178, v2
	v_mov_b32_e32 v179, v2
	v_mov_b32_e32 v180, v2
	v_mov_b32_e32 v181, v2
	v_mov_b32_e32 v182, v2
	v_mov_b32_e32 v183, v2
	v_mov_b32_e32 v184, v2
	v_mov_b32_e32 v185, v2
.LBB0_1223:
	s_add_i32 s51, s48, 0xfffe0080
	v_add_u32_e32 v38, 0x10000, v210
	v_add_u32_e32 v54, 0x14000, v210
	s_cmp_eq_u32 s50, 4
	ds_read_b128 v[26:29], v38
	ds_read_b128 v[30:33], v38 offset:1024
	ds_read_b128 v[34:37], v38 offset:2048
	ds_read_b128 v[38:41], v38 offset:3072
	ds_read_b128 v[42:45], v54
	s_waitcnt vmcnt(2)
	ds_read_b128 v[46:49], v54 offset:1024
	ds_read_b128 v[50:53], v54 offset:2048
	ds_read_b128 v[54:57], v54 offset:3072
	s_cselect_b32 s69, s38, s51
	s_cselect_b32 s52, s39, s49
	s_or_b32 s51, s69, 0x80
	s_cmp_eq_u32 s50, -2
	s_cselect_b64 s[62:63], -1, 0
	s_and_b64 s[62:63], s[36:37], s[62:63]
	v_cndmask_b32_e64 v58, 0, 1, s[62:63]
	s_or_b32 s53, s52, 0x8000
	v_readfirstlane_b32 s61, v58
	s_mov_b32 s62, s85
	ds_read_b128 v[58:61], v209
	ds_read_b128 v[62:65], v209 offset:1024
	ds_read_b128 v[66:69], v209 offset:2048
	ds_read_b128 v[70:73], v209 offset:3072
	ds_read_b128 v[162:165], v209 offset:4096
	ds_read_b128 v[174:177], v209 offset:5120
	ds_read_b128 v[186:189], v209 offset:6144
	ds_read_b128 v[190:193], v209 offset:7168
	s_add_i32 m0, s62, 0xc000
	s_mov_b32 s90, s66
	s_mov_b32 s91, s67
	s_mov_b32 s62, s85
	buffer_load_dwordx4 v0, s[88:91], s48 offen lds
	s_add_i32 m0, s62, 0xe000
	s_and_b32 s61, s61, 1
	buffer_load_dwordx4 v195, s[88:91], s48 offen lds
	s_cmp_lg_u32 s61, 0
	s_cbranch_scc1 .Lgr8
	s_waitcnt vmcnt(8)
; #define PG8_STAGE(bufoff, RS, soff, voff) do { _Pragma("unroll") for (int _i = 0; _i < 2; ++_i) \
;         __builtin_amdgcn_raw_ptr_buffer_load_lds(RS, (PG8_LAS void*)(lds + (bufoff) + sgpr_opaque(ldsw) + _i * 8192), 16, (int)(voff)[_i], (int)(soff), 0, 0); } while (0)
; #define PG8_LDA(dst, b, h) do { _Pragma("unroll") for (int m = 0; m < 4; ++m) _Pragma("unroll") for (int k = 0; k < 2; ++k) dst[m][k] = *(const PG8_LAS f16x8*)(lds + PG8_SA(b, h) + aoff + m * 2048 + k * 1024); } while (0)
; #define PG8_LDB(dst, b, h) do { _Pragma("unroll") for (int n = 0; n < 2; ++n) _Pragma("unroll") for (int k = 0; k < 2; ++k) dst[n][k] = *(const PG8_LAS f16x8*)(lds + PG8_SB(b, h) + boff + n * 2048 + k * 1024); } while (0)
; #define PG8_WAIT_L(n) asm volatile("s_waitcnt lgkmcnt(" #n ")" ::: "memory")
; #define PG8_BAR __builtin_amdgcn_s_barrier()
; #define PG8_SCHED __builtin_amdgcn_sched_barrier(0)
; template <class Epi, class Sched, bool ALIGN_EPI = false, bool SP2 = false, bool I8 = false, bool ATILED = false>
; __device__ __forceinline__ void gemm_phase(PG8_LAS unsigned char* lds, const Gemm g, const Sched& S, const Epi& E, const int wid) {
;     ...
;             PG8_LDB(B0, 0, 0); PG8_LDB(B1, 0, 1); PG8_SCHED; PG8_LDA(At, 0, 0); PG8_STAGE(PG8_SA(1, 1), rsA, a1 + hstepA, voffA);
;             PG8_WAIT_VG; PG8_WAIT_L(0); PG8_BAR; PG8_MMA(0, 0, At, B0); PG8_MMA(0, 1, At, B1); PG8_BAR; PG8_SCHED;
;             PG8_LDA(At, 0, 1); PG8_STAGE(PG8_SB(0, 0), rsB, b2, voffB); PG8_STAGE(PG8_SB(0, 1), rsB, b2 + hstep, voffB); PG8_STAGE(PG8_SA(0, 0), rsA, a2, voffA);
.Lgr8:
	s_waitcnt vmcnt(36)
	s_waitcnt lgkmcnt(0)
	s_barrier
	s_setprio 1
	s_waitcnt lgkmcnt(7)
	v_mfma_i32_16x16x64_i8 v[182:185], v[26:29], v[58:61], v[182:185]
	v_mfma_i32_16x16x64_i8 v[178:181], v[34:37], v[58:61], v[178:181]
	s_waitcnt lgkmcnt(5)
	v_mfma_i32_16x16x64_i8 v[158:161], v[26:29], v[66:69], v[158:161]
	v_mfma_i32_16x16x64_i8 v[154:157], v[34:37], v[66:69], v[154:157]
	s_waitcnt lgkmcnt(3)
	v_mfma_i32_16x16x64_i8 v[142:145], v[26:29], v[162:165], v[142:145]
	v_mfma_i32_16x16x64_i8 v[138:141], v[34:37], v[162:165], v[138:141]
	s_waitcnt lgkmcnt(1)
	v_mfma_i32_16x16x64_i8 v[126:129], v[26:29], v[186:189], v[126:129]
	v_mfma_i32_16x16x64_i8 v[122:125], v[34:37], v[186:189], v[122:125]
	v_mfma_i32_16x16x64_i8 v[182:185], v[30:33], v[62:65], v[182:185]
	v_mfma_i32_16x16x64_i8 v[178:181], v[38:41], v[62:65], v[178:181]
	v_mfma_i32_16x16x64_i8 v[158:161], v[30:33], v[70:73], v[158:161]
	v_mfma_i32_16x16x64_i8 v[154:157], v[38:41], v[70:73], v[154:157]
	v_mfma_i32_16x16x64_i8 v[142:145], v[30:33], v[174:177], v[142:145]
	v_mfma_i32_16x16x64_i8 v[138:141], v[38:41], v[174:177], v[138:141]
	s_waitcnt lgkmcnt(0)
	v_mfma_i32_16x16x64_i8 v[126:129], v[30:33], v[190:193], v[126:129]
	v_mfma_i32_16x16x64_i8 v[122:125], v[38:41], v[190:193], v[122:125]
	s_setprio 0
	s_setprio 1
	v_mfma_i32_16x16x64_i8 v[170:173], v[42:45], v[58:61], v[170:173]
	v_mfma_i32_16x16x64_i8 v[58:61], v[50:53], v[58:61], v[166:169]
	v_mfma_i32_16x16x64_i8 v[170:173], v[46:49], v[62:65], v[170:173]
	v_mfma_i32_16x16x64_i8 v[58:61], v[54:57], v[62:65], v[58:61]
	v_mfma_i32_16x16x64_i8 v[62:65], v[42:45], v[66:69], v[150:153]
	v_mfma_i32_16x16x64_i8 v[66:69], v[50:53], v[66:69], v[146:149]
	v_mfma_i32_16x16x64_i8 v[130:133], v[50:53], v[162:165], v[130:133]
	v_mfma_i32_16x16x64_i8 v[118:121], v[42:45], v[186:189], v[118:121]
	v_mfma_i32_16x16x64_i8 v[114:117], v[50:53], v[186:189], v[114:117]
	v_mfma_i32_16x16x64_i8 v[62:65], v[46:49], v[70:73], v[62:65]
	v_mfma_i32_16x16x64_i8 v[66:69], v[54:57], v[70:73], v[66:69]
	v_mfma_i32_16x16x64_i8 v[70:73], v[42:45], v[162:165], v[134:137]
	v_mfma_i32_16x16x64_i8 v[130:133], v[54:57], v[174:177], v[130:133]
	v_mfma_i32_16x16x64_i8 v[118:121], v[46:49], v[190:193], v[118:121]
	v_mfma_i32_16x16x64_i8 v[114:117], v[54:57], v[190:193], v[114:117]
	v_mfma_i32_16x16x64_i8 v[70:73], v[46:49], v[174:177], v[70:73]
	s_setprio 0
	s_barrier
	s_mov_b32 s62, s85
	ds_read_b128 v[134:137], v209 offset:16384
	ds_read_b128 v[146:149], v209 offset:17408
	ds_read_b128 v[150:153], v209 offset:18432
	ds_read_b128 v[162:165], v209 offset:19456
	ds_read_b128 v[166:169], v209 offset:20480
	ds_read_b128 v[174:177], v209 offset:21504
	ds_read_b128 v[186:189], v209 offset:22528
	ds_read_b128 v[190:193], v209 offset:23552
	s_add_i32 m0, s62, 0x10000
	s_mov_b32 s62, s85
	buffer_load_dwordx4 v194, s[64:67], s52 offen lds
	s_add_i32 m0, s62, 0x12000
	s_mov_b32 s63, s85
	buffer_load_dwordx4 v196, s[64:67], s52 offen lds
	s_add_i32 s62, s52, 0x4000
	s_add_i32 m0, s63, 0x14000
	s_mov_b32 s63, s85
	buffer_load_dwordx4 v194, s[64:67], s62 offen lds
	s_add_i32 m0, s63, 0x16000
	s_nop 0
	buffer_load_dwordx4 v196, s[64:67], s62 offen lds
	s_mov_b32 s62, s85
	s_mov_b32 m0, s62
	s_mov_b32 s62, s85
	buffer_load_dwordx4 v0, s[88:91], s69 offen lds
	s_add_i32 m0, s62, 0x2000
	s_nop 0
	buffer_load_dwordx4 v195, s[88:91], s69 offen lds
	s_cmp_lg_u32 s61, 0
	s_cbranch_scc1 .Lgr9
	s_waitcnt vmcnt(8)

; #define PG8_STAGE(bufoff, RS, soff, voff) do { _Pragma("unroll") for (int _i = 0; _i < 2; ++_i) \
;         __builtin_amdgcn_raw_ptr_buffer_load_lds(RS, (PG8_LAS void*)(lds + (bufoff) + sgpr_opaque(ldsw) + _i * 8192), 16, (int)(voff)[_i], (int)(soff), 0, 0); } while (0)
; #define PG8_LDA(dst, b, h) do { _Pragma("unroll") for (int m = 0; m < 4; ++m) _Pragma("unroll") for (int k = 0; k < 2; ++k) dst[m][k] = *(const PG8_LAS f16x8*)(lds + PG8_SA(b, h) + aoff + m * 2048 + k * 1024); } while (0)
; #define PG8_LDB(dst, b, h) do { _Pragma("unroll") for (int n = 0; n < 2; ++n) _Pragma("unroll") for (int k = 0; k < 2; ++k) dst[n][k] = *(const PG8_LAS f16x8*)(lds + PG8_SB(b, h) + boff + n * 2048 + k * 1024); } while (0)
; #define PG8_WAIT_L(n) asm volatile("s_waitcnt lgkmcnt(" #n ")" ::: "memory")
; #define PG8_BAR __builtin_amdgcn_s_barrier()
; #define PG8_SCHED __builtin_amdgcn_sched_barrier(0)
; template <class Epi, class Sched, bool ALIGN_EPI = false, bool SP2 = false, bool I8 = false, bool ATILED = false>
; __device__ __forceinline__ void gemm_phase(PG8_LAS unsigned char* lds, const Gemm g, const Sched& S, const Epi& E, const int wid) {
;     ...
;             PG8_WAIT_VG; PG8_WAIT_L(0); PG8_BAR; PG8_MMA(1, 0, At, B0); PG8_MMA(1, 1, At, B1); PG8_BAR; PG8_SCHED;
;             PG8_LDB(B0, 1, 0); PG8_LDB(B1, 1, 1); PG8_SCHED; PG8_LDA(At, 1, 0); PG8_STAGE(PG8_SA(0, 1), rsA, a2 + hstepA, voffA);
;             PG8_WAIT_VG; PG8_WAIT_L(0); PG8_BAR; PG8_MMA(0, 0, At, B0); PG8_MMA(0, 1, At, B1); PG8_BAR; PG8_SCHED;
;             PG8_LDA(At, 1, 1); PG8_STAGE(PG8_SB(1, 0), rsB, b3, voffB); PG8_STAGE(PG8_SB(1, 1), rsB, b3 + hstep, voffB); PG8_STAGE(PG8_SA(1, 0), rsA, a3, voffA);
;             PG8_WAIT_VG; PG8_WAIT_L(0); PG8_BAR; PG8_MMA(1, 0, At, B0); PG8_MMA(1, 1, At, B1); PG8_BAR; PG8_SCHED;
.Lgr10:
	s_waitcnt vmcnt(36)
	s_waitcnt lgkmcnt(0)
	s_barrier
	s_setprio 1
	s_waitcnt lgkmcnt(7)
	v_mfma_i32_16x16x64_i8 v[134:137], v[42:45], v[82:85], v[182:185]
	s_waitcnt lgkmcnt(6)
	v_mfma_i32_16x16x64_i8 v[182:185], v[46:49], v[86:89], v[134:137]
	v_mfma_i32_16x16x64_i8 v[134:137], v[50:53], v[82:85], v[178:181]
	v_mfma_i32_16x16x64_i8 v[178:181], v[54:57], v[86:89], v[134:137]
	s_waitcnt lgkmcnt(5)
	v_mfma_i32_16x16x64_i8 v[134:137], v[42:45], v[98:101], v[158:161]
	s_waitcnt lgkmcnt(4)
	v_mfma_i32_16x16x64_i8 v[158:161], v[46:49], v[102:105], v[134:137]
	v_mfma_i32_16x16x64_i8 v[134:137], v[50:53], v[98:101], v[154:157]
	v_mfma_i32_16x16x64_i8 v[154:157], v[54:57], v[102:105], v[134:137]
	s_waitcnt lgkmcnt(3)
	v_mfma_i32_16x16x64_i8 v[134:137], v[42:45], v[212:215], v[142:145]
	s_waitcnt lgkmcnt(2)
	v_mfma_i32_16x16x64_i8 v[142:145], v[46:49], v[216:219], v[134:137]
	v_mfma_i32_16x16x64_i8 v[134:137], v[50:53], v[212:215], v[138:141]
	s_waitcnt lgkmcnt(1)
	v_mfma_i32_16x16x64_i8 v[126:129], v[42:45], v[220:223], v[126:129]
	v_mfma_i32_16x16x64_i8 v[122:125], v[50:53], v[220:223], v[122:125]
	v_mfma_i32_16x16x64_i8 v[138:141], v[54:57], v[216:219], v[134:137]
	s_waitcnt lgkmcnt(0)
	v_mfma_i32_16x16x64_i8 v[126:129], v[46:49], v[224:227], v[126:129]
	v_mfma_i32_16x16x64_i8 v[122:125], v[54:57], v[224:227], v[122:125]
	s_setprio 0
	s_setprio 1
	v_mfma_i32_16x16x64_i8 v[58:61], v[186:189], v[82:85], v[58:61]
	v_mfma_i32_16x16x64_i8 v[166:169], v[190:193], v[86:89], v[58:61]
	v_mfma_i32_16x16x64_i8 v[58:61], v[162:165], v[98:101], v[62:65]
	v_mfma_i32_16x16x64_i8 v[150:153], v[174:177], v[102:105], v[58:61]
	v_mfma_i32_16x16x64_i8 v[58:61], v[186:189], v[98:101], v[66:69]
	v_mfma_i32_16x16x64_i8 v[134:137], v[162:165], v[82:85], v[170:173]
	v_mfma_i32_16x16x64_i8 v[146:149], v[190:193], v[102:105], v[58:61]
	v_mfma_i32_16x16x64_i8 v[58:61], v[162:165], v[212:215], v[70:73]
	v_mfma_i32_16x16x64_i8 v[170:173], v[174:177], v[86:89], v[134:137]
	v_mfma_i32_16x16x64_i8 v[134:137], v[174:177], v[216:219], v[58:61]
	v_mfma_i32_16x16x64_i8 v[58:61], v[186:189], v[212:215], v[130:133]
	v_mfma_i32_16x16x64_i8 v[130:133], v[190:193], v[216:219], v[58:61]
	v_mfma_i32_16x16x64_i8 v[58:61], v[162:165], v[220:223], v[118:121]
	v_mfma_i32_16x16x64_i8 v[118:121], v[174:177], v[224:227], v[58:61]
	v_mfma_i32_16x16x64_i8 v[58:61], v[186:189], v[220:223], v[114:117]
	v_mfma_i32_16x16x64_i8 v[114:117], v[190:193], v[224:227], v[58:61]
	s_setprio 0
	s_barrier
	s_mov_b32 s62, s85
	s_nop 3
	ds_read_b128 v[58:61], v209 offset:49152
	ds_read_b128 v[62:65], v209 offset:50176
	ds_read_b128 v[66:69], v209 offset:51200
	ds_read_b128 v[70:73], v209 offset:52224
	ds_read_b128 v[212:215], v209 offset:53248
	ds_read_b128 v[216:219], v209 offset:54272
	ds_read_b128 v[220:223], v209 offset:55296
	ds_read_b128 v[224:227], v209 offset:56320
	s_add_i32 m0, s62, 0x18000
	s_mov_b32 s62, s85
	buffer_load_dwordx4 v194, s[64:67], s53 offen lds
	s_add_i32 m0, s62, 0x1a000
	s_add_i32 s52, s52, 0xc000
	buffer_load_dwordx4 v196, s[64:67], s53 offen lds
	s_mov_b32 s53, s85
	s_add_i32 m0, s53, 0x1c000
	s_mov_b32 s53, s85
	buffer_load_dwordx4 v194, s[64:67], s52 offen lds
	s_add_i32 m0, s53, 0x1e000
	s_nop 0
	buffer_load_dwordx4 v196, s[64:67], s52 offen lds
	s_mov_b32 s52, s85
	s_add_i32 m0, s52, 0x8000
	s_mov_b32 s52, s85
	buffer_load_dwordx4 v0, s[88:91], s51 offen lds
	s_add_i32 m0, s52, 0xa000
	s_nop 0
	buffer_load_dwordx4 v195, s[88:91], s51 offen lds
	s_cmp_lg_u32 s61, 0
	s_cbranch_scc1 .Lgr11
	s_waitcnt vmcnt(8)
.Lgr11:
	s_waitcnt vmcnt(36)
	s_waitcnt lgkmcnt(0)
	s_barrier
	s_setprio 1
	s_waitcnt lgkmcnt(7)
	v_mfma_i32_16x16x64_i8 v[82:85], v[42:45], v[58:61], v[110:113]
	s_waitcnt lgkmcnt(6)
	v_mfma_i32_16x16x64_i8 v[110:113], v[46:49], v[62:65], v[82:85]
	v_mfma_i32_16x16x64_i8 v[82:85], v[50:53], v[58:61], v[106:109]
	v_mfma_i32_16x16x64_i8 v[106:109], v[54:57], v[62:65], v[82:85]
	s_waitcnt lgkmcnt(5)
	v_mfma_i32_16x16x64_i8 v[82:85], v[42:45], v[66:69], v[94:97]
	s_waitcnt lgkmcnt(4)
	v_mfma_i32_16x16x64_i8 v[94:97], v[46:49], v[70:73], v[82:85]
	v_mfma_i32_16x16x64_i8 v[82:85], v[50:53], v[66:69], v[90:93]
	s_waitcnt lgkmcnt(3)
	v_mfma_i32_16x16x64_i8 v[78:81], v[42:45], v[212:215], v[78:81]
	v_mfma_i32_16x16x64_i8 v[74:77], v[50:53], v[212:215], v[74:77]
	s_waitcnt lgkmcnt(1)
	v_mfma_i32_16x16x64_i8 v[14:17], v[42:45], v[220:223], v[14:17]
	v_mfma_i32_16x16x64_i8 v[10:13], v[50:53], v[220:223], v[10:13]
	v_mfma_i32_16x16x64_i8 v[90:93], v[54:57], v[70:73], v[82:85]
	v_mfma_i32_16x16x64_i8 v[78:81], v[46:49], v[216:219], v[78:81]
	v_mfma_i32_16x16x64_i8 v[74:77], v[54:57], v[216:219], v[74:77]
	s_waitcnt lgkmcnt(0)
	v_mfma_i32_16x16x64_i8 v[14:17], v[46:49], v[224:227], v[14:17]
	v_mfma_i32_16x16x64_i8 v[10:13], v[54:57], v[224:227], v[10:13]
	s_setprio 0
	s_setprio 1
	v_mfma_i32_16x16x64_i8 v[26:29], v[162:165], v[58:61], v[26:29]
	v_mfma_i32_16x16x64_i8 v[102:105], v[174:177], v[62:65], v[26:29]
	v_mfma_i32_16x16x64_i8 v[26:29], v[186:189], v[58:61], v[30:33]
	v_mfma_i32_16x16x64_i8 v[98:101], v[190:193], v[62:65], v[26:29]
	v_mfma_i32_16x16x64_i8 v[26:29], v[162:165], v[66:69], v[34:37]
	v_mfma_i32_16x16x64_i8 v[86:89], v[174:177], v[70:73], v[26:29]
	v_mfma_i32_16x16x64_i8 v[26:29], v[186:189], v[66:69], v[38:41]
	v_mfma_i32_16x16x64_i8 v[22:25], v[162:165], v[212:215], v[22:25]
	v_mfma_i32_16x16x64_i8 v[18:21], v[186:189], v[212:215], v[18:21]
	v_mfma_i32_16x16x64_i8 v[6:9], v[162:165], v[220:223], v[6:9]
	v_mfma_i32_16x16x64_i8 v[2:5], v[186:189], v[220:223], v[2:5]
	v_mfma_i32_16x16x64_i8 v[82:85], v[190:193], v[70:73], v[26:29]
	v_mfma_i32_16x16x64_i8 v[22:25], v[174:177], v[216:219], v[22:25]
	v_mfma_i32_16x16x64_i8 v[18:21], v[190:193], v[216:219], v[18:21]
	v_mfma_i32_16x16x64_i8 v[6:9], v[174:177], v[224:227], v[6:9]
	v_mfma_i32_16x16x64_i8 v[2:5], v[190:193], v[224:227], v[2:5]
	s_setprio 0
	s_barrier
	s_add_i32 s50, s50, 2
	s_addk_i32 s48, 0x100
	s_add_i32 s49, s49, 0x10000
	s_cmp_gt_u32 s50, 5
	s_cbranch_scc0 .LBB0_1223
	s_and_b64 vcc, exec, s[56:57]
	s_cbranch_vccz .LBB0_1226
	s_barrier

;     __host__ __device__ bool next(int i, Unit& u) const { if (!so.next(i / 3, u)) return false; u.pn += 4 * (i % 3); u.idx = i; return true; }
; #define PG8_BAR __builtin_amdgcn_s_barrier()
; template <class Epi, class Sched, bool ALIGN_EPI = false, bool SP2 = false, bool I8 = false, bool ATILED = false>
; __device__ __forceinline__ void gemm_phase(PG8_LAS unsigned char* lds, const Gemm g, const Sched& S, const Epi& E, const int wid) {
;     ...
;     for (int i = 0; i < 2; ++i) { int R, C; stage_rc(tid * 16 + i * 8192, R, C); const int Rb = Epi::PERM ? ((R & ~31) + perm32(R & 31)) : R;
;         voffA[i] = (unsigned)(R * (ATILED ? BK : K) + C) * 2u; voffB[i] = (unsigned)(Rb * K + C) * 2u; }
;     const unsigned kstep = (unsigned)(BK * 2);
;     const unsigned hstep = (unsigned)HALF * K * 2;
;     const unsigned tstep = 2 * hstep;
;     const unsigned kstepA = ATILED ? (unsigned)(BM * BK * 2) : kstep, hstepA = ATILED ? (unsigned)(HALF * BK * 2) : hstep, tstepA = ATILED ? (unsigned)nt * (unsigned)(BM * BK * 2) : tstep;
;     const __amdgpu_buffer_rsrc_t rsA = __builtin_amdgcn_make_buffer_rsrc((void*)g.A, 0, 0x7fffffff, 0x00020000), rsB = __builtin_amdgcn_make_buffer_rsrc((void*)g.Bt, 0, 0x7fffffff, 0x00020000);
;     const unsigned ldsw = (unsigned)wid * 1024u;
;     const int aoff = lds_byte(wr * 64 + fr, fq * 8), boff = lds_byte(wc * 32 + fr, fq * 8);
;     ...
;     Unit cur, nxt; int ui = 0;
;     if (!S.next(0, cur)) return;
;     f32x4 acc[2][2][4][2];
; #pragma unroll
;     for (int a = 0; a < 2; ++a)
; #pragma unroll
;         for (int b = 0; b < 2; ++b)
; #pragma unroll
;             for (int m = 0; m < 4; ++m)
; #pragma unroll
;                 for (int n = 0; n < 2; ++n) acc[a][b][m][n] = (f32x4){0.f, 0.f, 0.f, 0.f};
;     f16x8 At[4][2], B0[2][2], B1[2][2];
;     unsigned cA = (unsigned)cur.pm * tstepA + (unsigned)(cur.pm >> 4) * g.gapA, cB = (unsigned)cur.pn * tstep;
;     S.a_ready(cur);
;     if constexpr (SP2) {
;         PG8_STAGE(PG8_SB(0, 0), rsB, cB, voffB); PG8_STAGE(PG8_SB(0, 1), rsB, cB + hstep, voffB); PG8_STAGE(PG8_SA(0, 0), rsA, cA, voffA); PG8_STAGE(PG8_SA(0, 1), rsA, cA + hstepA, voffA);
;         if (wr == 1) PG8_BAR;
;         PG8_WAIT_V(2); PG8_BAR;
;         PG8_STAGE(PG8_SB(1, 0), rsB, cB + kstep, voffB); PG8_STAGE(PG8_SA(1, 0), rsA, cA + kstepA, voffA); PG8_STAGE(PG8_SB(1, 1), rsB, cB + hstep + kstep, voffB);
;         PG8_WAIT_V(6); PG8_BAR;
.LBB0_1598:
	v_readlane_b32 s26, v254, 20
	v_readlane_b32 s27, v254, 21
	s_andn2_b64 vcc, exec, s[26:27]
	s_waitcnt lgkmcnt(0)
	s_barrier
	v_mbcnt_lo_u32_b32 v0, -1, 0
	v_mbcnt_hi_u32_b32 v0, -1, v0
	s_cbranch_vccnz .LBB0_1618
	v_lshl_add_u32 v2, v0, 4, s85
	v_ashrrev_i32_e32 v3, 31, v2
	v_lshrrev_b32_e32 v3, 22, v3
	v_add_u32_e32 v3, v2, v3
	v_ashrrev_i32_e32 v3, 10, v3
	s_waitcnt vmcnt(0)
	v_mul_i32_i24_e32 v4, 0x400, v3
	v_sub_u32_e32 v4, v2, v4
	v_lshrrev_b32_e32 v5, 4, v4
	v_bitop3_b32 v4, v5, v4, 32 bitop3:0x6c
	s_ashr_i32 s49, s48, 31
	v_ashrrev_i32_e32 v6, 31, v4
	s_lshl_b64 s[26:27], s[48:49], 22
	v_lshrrev_b32_e32 v6, 26, v6
	s_add_u32 s26, s46, s26
	v_lshlrev_b32_e32 v5, 3, v3
	v_add_u32_e32 v6, v4, v6
	s_addc_u32 s27, s47, s27
	v_and_b32_e32 v5, -16, v5
	v_ashrrev_i32_e32 v7, 6, v6
	v_and_b32_e32 v6, 0xc0, v6
	s_add_u32 s64, s26, 0x1f700000
	v_add_u32_e32 v5, v7, v5
	v_sub_u32_e32 v4, v4, v6
	s_addc_u32 s26, s27, 0
	v_lshlrev_b32_e32 v3, 5, v3
	v_ashrrev_i16_sdwa v4, v232, sext(v4) dst_sel:DWORD dst_unused:UNUSED_PAD src0_sel:DWORD src1_sel:BYTE_0
	v_lshlrev_b32_e32 v6, 1, v5
	v_lshrrev_b32_e32 v8, 2, v5
	v_and_b32_e32 v7, 3, v7
	s_mov_b32 s27, 0x3fffe0
	v_and_b32_e32 v3, 32, v3
	v_bfe_i32 v4, v4, 0, 16
	v_and_b32_e32 v6, 24, v6
	v_and_b32_e32 v8, 4, v8
	v_and_or_b32 v7, v5, s27, v7
	v_or3_b32 v6, v7, v8, v6
	v_add_lshl_u32 v3, v3, v4, 1
	v_add_u32_e32 v2, 0x2000, v2
	v_lshl_add_u32 v172, v5, 10, v3
	v_mbcnt_lo_u32_b32 v173, -1, 0
	v_mbcnt_hi_u32_b32 v173, -1, v173
	v_lshl_add_u32 v173, v173, 4, s85
	v_ashrrev_i32_e32 v3, 31, v2
	v_lshrrev_b32_e32 v3, 22, v3
	v_add_u32_e32 v3, v2, v3
	v_ashrrev_i32_e32 v3, 10, v3
	v_mul_i32_i24_e32 v4, 0x400, v3
	v_sub_u32_e32 v2, v2, v4
	v_lshrrev_b32_e32 v4, 4, v2
	v_bitop3_b32 v2, v4, v2, 32 bitop3:0x6c
	v_ashrrev_i32_e32 v5, 31, v2
	v_lshrrev_b32_e32 v5, 26, v5
	v_add_u32_e32 v5, v2, v5
	v_ashrrev_i32_e32 v6, 6, v5
	v_and_b32_e32 v5, 0xffc0, v5
	v_sub_u32_e32 v2, v2, v5
	v_lshlrev_b32_e32 v4, 3, v3
	v_lshrrev_b16_e32 v5, 7, v2
	v_and_b32_e32 v4, -16, v4
	v_and_b32_e32 v5, 1, v5
	v_add_u32_e32 v4, v6, v4
	v_add_u16_e32 v2, v2, v5
	s_and_b32 s65, s26, 0xffff
	s_mov_b32 s26, s85
	v_lshlrev_b32_e32 v3, 5, v3
	v_ashrrev_i16_sdwa v2, v232, sext(v2) dst_sel:DWORD dst_unused:UNUSED_PAD src0_sel:DWORD src1_sel:BYTE_0
	v_lshlrev_b32_e32 v5, 1, v4
	v_lshrrev_b32_e32 v7, 2, v4
	v_and_b32_e32 v6, 3, v6
	v_and_b32_e32 v3, 32, v3
	v_bfe_i32 v2, v2, 0, 16
	v_and_b32_e32 v5, 24, v5
	v_and_b32_e32 v7, 4, v7
	v_and_or_b32 v6, v4, s27, v6
	s_add_i32 m0, s26, 0x10000
	v_readlane_b32 s27, v254, 51
	s_bfe_u32 s100, s27, 0x10011
	s_bfe_u32 s101, s27, 0x10007
	s_and_b32 s27, s27, 0xfffc0000
	s_lshl_b32 s100, s100, 14
	s_lshl_b32 s101, s101, 15
	s_or_b32 s27, s27, s100
	s_or_b32 s27, s27, s101
	s_mov_b32 s26, s85
	v_or3_b32 v5, v6, v7, v5
	v_add_lshl_u32 v2, v3, v2, 1
	v_mbcnt_lo_u32_b32 v175, -1, 0
	v_mbcnt_hi_u32_b32 v175, -1, v175
	v_lshl_add_u32 v175, v175, 4, s85
	v_add_u32_e32 v175, 0x2000, v175
	s_mov_b32 s90, s66
	buffer_load_dwordx4 v173, s[64:67], s27 offen lds
	s_add_i32 m0, s26, 0x12000
	s_mov_b32 s26, s85
	buffer_load_dwordx4 v175, s[64:67], s27 offen lds
	s_add_i32 m0, s26, 0x14000
	v_readlane_b32 s27, v254, 45
	s_bfe_u32 s100, s27, 0x10011
	s_bfe_u32 s101, s27, 0x10007
	s_and_b32 s27, s27, 0xfffc0000
	s_lshl_b32 s100, s100, 14
	s_lshl_b32 s101, s101, 15
	s_or_b32 s27, s27, s100
	s_or_b32 s27, s27, s101
	s_mov_b32 s26, s85
	s_mov_b32 s91, s67
	v_lshl_add_u32 v174, v4, 10, v2
	v_readlane_b32 s22, v253, 31
	v_readlane_b32 s23, v253, 32
	buffer_load_dwordx4 v173, s[64:67], s27 offen lds
	s_add_i32 m0, s26, 0x16000
	s_mov_b32 s26, s85
	buffer_load_dwordx4 v175, s[64:67], s27 offen lds
	s_mov_b32 m0, s26
	v_readlane_b32 s27, v254, 49
	s_mov_b32 s26, s85
	s_and_b64 vcc, exec, s[22:23]
	s_nop 2
	buffer_load_dwordx4 v172, s[88:91], s27 offen lds
	s_add_i32 m0, s26, 0x2000
	s_mov_b32 s26, s85
	buffer_load_dwordx4 v174, s[88:91], s27 offen lds
	s_add_i32 m0, s26, 0x4000
	v_readlane_b32 s27, v254, 47
	s_mov_b32 s26, s85
	s_nop 3
	buffer_load_dwordx4 v172, s[88:91], s27 offen lds
	s_add_i32 m0, s26, 0x6000
	s_nop 0
	buffer_load_dwordx4 v174, s[88:91], s27 offen lds
	s_cbranch_vccnz .LBB0_1601
	s_barrier
.LBB0_1601:
	s_mov_b32 s26, s85
	s_add_u32 s36, s44, 0xe800000
	s_waitcnt vmcnt(2)
	s_barrier
	s_addc_u32 s37, s45, 0
	s_add_i32 m0, s26, 0x18000
	v_readlane_b32 s27, v254, 48
	s_bfe_u32 s100, s27, 0x10011
	s_bfe_u32 s101, s27, 0x10007
	s_and_b32 s27, s27, 0xfffc0000
	s_lshl_b32 s100, s100, 14
	s_lshl_b32 s101, s101, 15
	s_or_b32 s27, s27, s100
	s_or_b32 s27, s27, s101
	s_mov_b32 s26, s85
	v_and_b32_e32 v176, 15, v0
	v_or_b32_e32 v177, s96, v176
	v_lshlrev_b32_e32 v4, 6, v177
	v_and_b32_e32 v5, 48, v0
	buffer_load_dwordx4 v173, s[64:67], s27 offen lds
	s_add_i32 m0, s26, 0x1a000
	s_mov_b32 s26, s85
	buffer_load_dwordx4 v175, s[64:67], s27 offen lds
	s_add_i32 m0, s26, 0x8000
	v_readlane_b32 s27, v254, 50
	s_mov_b32 s26, s85
	v_ashrrev_i32_e32 v3, 6, v0
	v_ashrrev_i32_e32 v2, 1, v0
	v_lshlrev_b32_e32 v7, 2, v177
	v_and_b32_e32 v2, -8, v2
	buffer_load_dwordx4 v172, s[88:91], s27 offen lds
	s_add_i32 m0, s26, 0xa000
	s_mov_b32 s26, s85
	buffer_load_dwordx4 v174, s[88:91], s27 offen lds
	s_add_i32 m0, s26, 0x1c000
	v_readlane_b32 s27, v254, 52
	s_bfe_u32 s100, s27, 0x10011
	s_bfe_u32 s101, s27, 0x10007
	s_and_b32 s27, s27, 0xfffc0000
	s_lshl_b32 s100, s100, 14
	s_lshl_b32 s101, s101, 15
	s_or_b32 s27, s27, s100
	s_or_b32 s27, s27, s101
	s_mov_b32 s26, s85
	v_and_b32_e32 v7, 32, v7
	v_lshlrev_b32_e32 v0, 2, v0
	v_and_b32_e32 v0, 32, v0
	s_mov_b32 s46, 0
	buffer_load_dwordx4 v173, s[64:67], s27 offen lds
	s_add_i32 m0, s26, 0x1e000
	s_movk_i32 s26, 0x3c0
	buffer_load_dwordx4 v175, s[64:67], s27 offen lds
	v_and_or_b32 v4, v4, s26, v5
	v_readlane_b32 s26, v253, 60
	s_waitcnt vmcnt(6)
	v_readlane_b32 s44, v254, 44
	v_readlane_b32 s45, v254, 46
	v_lshl_add_u32 v6, v3, 10, s26
	v_readlane_b32 s26, v253, 62
	v_bitop3_b32 v178, v4, v6, v7 bitop3:0xde
	v_lshl_or_b32 v4, v176, 6, v5
	v_add_lshl_u32 v3, v3, s26, 10
	v_readlane_b32 s26, v253, 61
	v_bitop3_b32 v179, v4, v3, v0 bitop3:0xde
	v_readlane_b32 s50, v254, 51
	v_add_u32_e32 v180, s26, v2
	v_lshlrev_b32_e32 v0, 2, v180
	v_add_u32_e32 v181, 0x22400, v0
	v_add_u32_e32 v182, 0x24400, v0
	v_lshlrev_b32_e32 v0, 7, v177
	v_and_b32_e32 v2, 56, v180
	v_and_b32_e32 v0, 0x6780, v0
	v_lshl_add_u64 v[162:163], s[36:37], 0, v[0:1]
	v_lshlrev_b32_e32 v0, 1, v2
	v_readlane_b32 s49, v254, 49
	s_mov_b32 s51, 0
	s_barrier
	s_branch .LBB0_1604

;     __host__ __device__ bool next(int i, Unit& u) const { if (!so.next(i / 3, u)) return false; u.pn += 4 * (i % 3); u.idx = i; return true; }
; #define PG8_STAGE(bufoff, RS, soff, voff) do { _Pragma("unroll") for (int _i = 0; _i < 2; ++_i) \
;         __builtin_amdgcn_raw_ptr_buffer_load_lds(RS, (PG8_LAS void*)(lds + (bufoff) + sgpr_opaque(ldsw) + _i * 8192), 16, (int)(voff)[_i], (int)(soff), 0, 0); } while (0)
; #define PG8_LDA(dst, b, h) do { _Pragma("unroll") for (int m = 0; m < 4; ++m) _Pragma("unroll") for (int k = 0; k < 2; ++k) dst[m][k] = *(const PG8_LAS f16x8*)(lds + PG8_SA(b, h) + aoff + m * 2048 + k * 1024); } while (0)
; #define PG8_LDB(dst, b, h) do { _Pragma("unroll") for (int n = 0; n < 2; ++n) _Pragma("unroll") for (int k = 0; k < 2; ++k) dst[n][k] = *(const PG8_LAS f16x8*)(lds + PG8_SB(b, h) + boff + n * 2048 + k * 1024); } while (0)
; template <class Epi, class Sched, bool ALIGN_EPI = false, bool SP2 = false, bool I8 = false, bool ATILED = false>
; __device__ __forceinline__ void gemm_phase(PG8_LAS unsigned char* lds, const Gemm g, const Sched& S, const Epi& E, const int wid) {
;     ...
;         const bool has_next = S.next(ui + 1, nxt);
;         const unsigned nA = has_next ? (unsigned)nxt.pm * tstepA + (unsigned)(nxt.pm >> 4) * g.gapA : cA, nB = has_next ? (unsigned)nxt.pn * tstep : cB;
;         for (int t = 0; t < nt; t += 2) {
;             const bool last = (t == nt - 2);
;             const unsigned a1 = cA + (unsigned)(t + 1) * kstepA;
;             const unsigned a2 = last ? nA : cA + (unsigned)(t + 2) * kstepA, b2 = last ? nB : cB + (unsigned)(t + 2) * kstep;
;             const unsigned a3 = a2 + kstepA, b3 = b2 + kstep;
;             if (last && has_next) S.a_ready(nxt);
;             if constexpr (SP2) {
;             const int grace = __builtin_amdgcn_readfirstlane((PG8_GRACE && Epi::NSTORE > 0 && t == 0 && ui > 0) ? 1 : 0);
;     ...
;             PG8_LDB(B0, 0, 0); PG8_LDB(B1, 0, 1); PG8_SCHED; PG8_LDA(At, 0, 0); PG8_STAGE(PG8_SA(1, 1), rsA, a1 + hstepA, voffA);
;     ...
; #pragma unroll
;         for (int a = 0; a < 2; ++a)
; #pragma unroll
;             for (int b = 0; b < 2; ++b)
; #pragma unroll
;                 for (int m = 0; m < 4; ++m)
; #pragma unroll
;                     for (int n = 0; n < 2; ++n) acc[a][b][m][n] = (f32x4){0.f, 0.f, 0.f, 0.f};
;         cur = nxt; cA = nA; cB = nB; ++ui;
.LBB0_1610:
	s_lshl_b32 s42, s40, 18
	s_and_b64 s[38:39], s[34:35], exec
	s_cselect_b32 s47, s42, s49
	s_lshl_b32 s43, s27, 18
	s_and_b64 s[38:39], s[34:35], exec
	s_cselect_b32 s48, s43, s50
	s_cmp_lg_u32 s51, 0
	v_mov_b32_e32 v2, 0
	s_cselect_b64 s[38:39], -1, 0
	s_add_i32 s49, s49, 0x20080
	s_add_i32 s50, s50, 0x10000
	s_mov_b32 s51, -2
	v_mov_b32_e32 v3, v2
	v_mov_b32_e32 v4, v2
	v_mov_b32_e32 v5, v2
	v_mov_b32_e32 v6, v2
	v_mov_b32_e32 v7, v2
	v_mov_b32_e32 v8, v2
	v_mov_b32_e32 v9, v2
	v_mov_b32_e32 v18, v2
	v_mov_b32_e32 v19, v2
	v_mov_b32_e32 v20, v2
	v_mov_b32_e32 v21, v2
	v_mov_b32_e32 v22, v2
	v_mov_b32_e32 v23, v2
	v_mov_b32_e32 v24, v2
	v_mov_b32_e32 v25, v2
	v_mov_b32_e32 v34, v2
	v_mov_b32_e32 v35, v2
	v_mov_b32_e32 v36, v2
	v_mov_b32_e32 v37, v2
	v_mov_b32_e32 v38, v2
	v_mov_b32_e32 v39, v2
	v_mov_b32_e32 v40, v2
	v_mov_b32_e32 v41, v2
	v_mov_b32_e32 v50, v2
	v_mov_b32_e32 v51, v2
	v_mov_b32_e32 v52, v2
	v_mov_b32_e32 v53, v2
	v_mov_b32_e32 v54, v2
	v_mov_b32_e32 v55, v2
	v_mov_b32_e32 v56, v2
	v_mov_b32_e32 v57, v2
	v_mov_b32_e32 v10, v2
	v_mov_b32_e32 v11, v2
	v_mov_b32_e32 v12, v2
	v_mov_b32_e32 v13, v2
	v_mov_b32_e32 v14, v2
	v_mov_b32_e32 v15, v2
	v_mov_b32_e32 v16, v2
	v_mov_b32_e32 v17, v2
	v_mov_b32_e32 v26, v2
	v_mov_b32_e32 v27, v2
	v_mov_b32_e32 v28, v2
	v_mov_b32_e32 v29, v2
	v_mov_b32_e32 v30, v2
	v_mov_b32_e32 v31, v2
	v_mov_b32_e32 v32, v2
	v_mov_b32_e32 v33, v2
	v_mov_b32_e32 v42, v2
	v_mov_b32_e32 v43, v2
	v_mov_b32_e32 v44, v2
	v_mov_b32_e32 v45, v2
	v_mov_b32_e32 v46, v2
	v_mov_b32_e32 v47, v2
	v_mov_b32_e32 v48, v2
	v_mov_b32_e32 v49, v2
	v_mov_b32_e32 v58, v2
	v_mov_b32_e32 v59, v2
	v_mov_b32_e32 v60, v2
	v_mov_b32_e32 v61, v2
	v_mov_b32_e32 v62, v2
	v_mov_b32_e32 v63, v2
	v_mov_b32_e32 v64, v2
	v_mov_b32_e32 v65, v2
	v_mov_b32_e32 v66, v2
	v_mov_b32_e32 v67, v2
	v_mov_b32_e32 v68, v2
	v_mov_b32_e32 v69, v2
	v_mov_b32_e32 v70, v2
	v_mov_b32_e32 v71, v2
	v_mov_b32_e32 v72, v2
	v_mov_b32_e32 v73, v2
	v_mov_b32_e32 v82, v2
	v_mov_b32_e32 v83, v2
	v_mov_b32_e32 v84, v2
	v_mov_b32_e32 v85, v2
	v_mov_b32_e32 v86, v2
	v_mov_b32_e32 v87, v2
	v_mov_b32_e32 v88, v2
	v_mov_b32_e32 v89, v2
	v_mov_b32_e32 v98, v2
	v_mov_b32_e32 v99, v2
	v_mov_b32_e32 v100, v2
	v_mov_b32_e32 v101, v2
	v_mov_b32_e32 v102, v2
	v_mov_b32_e32 v103, v2
	v_mov_b32_e32 v104, v2
	v_mov_b32_e32 v105, v2
	v_mov_b32_e32 v146, v2
	v_mov_b32_e32 v147, v2
	v_mov_b32_e32 v148, v2
	v_mov_b32_e32 v149, v2
	v_mov_b32_e32 v150, v2
	v_mov_b32_e32 v151, v2
	v_mov_b32_e32 v152, v2
	v_mov_b32_e32 v153, v2
	v_mov_b32_e32 v74, v2
	v_mov_b32_e32 v75, v2
	v_mov_b32_e32 v76, v2
	v_mov_b32_e32 v77, v2
	v_mov_b32_e32 v78, v2
	v_mov_b32_e32 v79, v2
	v_mov_b32_e32 v80, v2
	v_mov_b32_e32 v81, v2
	v_mov_b32_e32 v90, v2
	v_mov_b32_e32 v91, v2
	v_mov_b32_e32 v92, v2
	v_mov_b32_e32 v93, v2
	v_mov_b32_e32 v94, v2
	v_mov_b32_e32 v95, v2
	v_mov_b32_e32 v96, v2
	v_mov_b32_e32 v97, v2
	v_mov_b32_e32 v122, v2
	v_mov_b32_e32 v123, v2
	v_mov_b32_e32 v124, v2
	v_mov_b32_e32 v125, v2
	v_mov_b32_e32 v134, v2
	v_mov_b32_e32 v135, v2
	v_mov_b32_e32 v136, v2
	v_mov_b32_e32 v137, v2
	v_mov_b32_e32 v154, v2
	v_mov_b32_e32 v155, v2
	v_mov_b32_e32 v156, v2
	v_mov_b32_e32 v157, v2
	v_mov_b32_e32 v158, v2
	v_mov_b32_e32 v159, v2
	v_mov_b32_e32 v160, v2
	v_mov_b32_e32 v161, v2
.LBB0_1611:
	s_add_i32 s52, s49, 0xfffe0080
	v_add_u32_e32 v118, 0x10000, v179
	v_add_u32_e32 v142, 0x14000, v179
	s_cmp_eq_u32 s51, 4
	ds_read_b128 v[106:109], v118
	ds_read_b128 v[110:113], v118 offset:1024
	ds_read_b128 v[114:117], v118 offset:2048
	ds_read_b128 v[118:121], v118 offset:3072
	ds_read_b128 v[126:129], v142
	ds_read_b128 v[130:133], v142 offset:1024
	ds_read_b128 v[138:141], v142 offset:2048
	ds_read_b128 v[142:145], v142 offset:3072
	s_cselect_b32 s58, s47, s52
	s_cselect_b32 s53, s48, s50
	s_or_b32 s52, s58, 0x80
	s_cmp_eq_u32 s51, -2
	s_cselect_b64 s[54:55], -1, 0
	s_and_b64 s[54:55], s[38:39], s[54:55]
	v_cndmask_b32_e64 v164, 0, 1, s[54:55]
	s_or_b32 s54, s53, 0x8000
	v_readfirstlane_b32 s55, v164
	s_mov_b32 s59, s85
	ds_read_b128 v[164:167], v178
	ds_read_b128 v[168:171], v178 offset:1024
	ds_read_b128 v[184:187], v178 offset:2048
	ds_read_b128 v[188:191], v178 offset:3072
	ds_read_b128 v[192:195], v178 offset:4096
	ds_read_b128 v[208:211], v178 offset:5120
	ds_read_b128 v[212:215], v178 offset:6144
	ds_read_b128 v[216:219], v178 offset:7168
	s_add_i32 m0, s59, 0xc000
	s_mov_b32 s90, s66
	s_mov_b32 s91, s67
	s_mov_b32 s59, s85
	buffer_load_dwordx4 v172, s[88:91], s49 offen lds
	s_add_i32 m0, s59, 0xe000
	s_and_b32 s55, s55, 1
	buffer_load_dwordx4 v174, s[88:91], s49 offen lds
	s_cmp_lg_u32 s55, 0
	s_cbranch_scc1 .Lgr16
	s_waitcnt vmcnt(8)
; #define PG8_STAGE(bufoff, RS, soff, voff) do { _Pragma("unroll") for (int _i = 0; _i < 2; ++_i) \
;         __builtin_amdgcn_raw_ptr_buffer_load_lds(RS, (PG8_LAS void*)(lds + (bufoff) + sgpr_opaque(ldsw) + _i * 8192), 16, (int)(voff)[_i], (int)(soff), 0, 0); } while (0)
; #define PG8_LDA(dst, b, h) do { _Pragma("unroll") for (int m = 0; m < 4; ++m) _Pragma("unroll") for (int k = 0; k < 2; ++k) dst[m][k] = *(const PG8_LAS f16x8*)(lds + PG8_SA(b, h) + aoff + m * 2048 + k * 1024); } while (0)
; #define PG8_LDB(dst, b, h) do { _Pragma("unroll") for (int n = 0; n < 2; ++n) _Pragma("unroll") for (int k = 0; k < 2; ++k) dst[n][k] = *(const PG8_LAS f16x8*)(lds + PG8_SB(b, h) + boff + n * 2048 + k * 1024); } while (0)
; #define PG8_WAIT_L(n) asm volatile("s_waitcnt lgkmcnt(" #n ")" ::: "memory")
; #define PG8_BAR __builtin_amdgcn_s_barrier()
; #define PG8_SCHED __builtin_amdgcn_sched_barrier(0)
; template <class Epi, class Sched, bool ALIGN_EPI = false, bool SP2 = false, bool I8 = false, bool ATILED = false>
; __device__ __forceinline__ void gemm_phase(PG8_LAS unsigned char* lds, const Gemm g, const Sched& S, const Epi& E, const int wid) {
;     ...
;             PG8_LDB(B0, 0, 0); PG8_LDB(B1, 0, 1); PG8_SCHED; PG8_LDA(At, 0, 0); PG8_STAGE(PG8_SA(1, 1), rsA, a1 + hstepA, voffA);
;             PG8_WAIT_VG; PG8_WAIT_L(0); PG8_BAR; PG8_MMA(0, 0, At, B0); PG8_MMA(0, 1, At, B1); PG8_BAR; PG8_SCHED;
;             PG8_LDA(At, 0, 1); PG8_STAGE(PG8_SB(0, 0), rsB, b2, voffB); PG8_STAGE(PG8_SB(0, 1), rsB, b2 + hstep, voffB); PG8_STAGE(PG8_SA(0, 0), rsA, a2, voffA);
.Lgr16:
	s_waitcnt vmcnt(24)
	s_waitcnt lgkmcnt(0)
	s_barrier
	s_setprio 1
	s_waitcnt lgkmcnt(7)
	v_mfma_i32_16x16x64_i8 v[158:161], v[106:109], v[164:167], v[158:161]
	v_mfma_i32_16x16x64_i8 v[154:157], v[114:117], v[164:167], v[154:157]
	s_waitcnt lgkmcnt(5)
	v_mfma_i32_16x16x64_i8 v[134:137], v[106:109], v[184:187], v[134:137]
	v_mfma_i32_16x16x64_i8 v[122:125], v[114:117], v[184:187], v[122:125]
	s_waitcnt lgkmcnt(3)
	v_mfma_i32_16x16x64_i8 v[94:97], v[106:109], v[192:195], v[94:97]
	v_mfma_i32_16x16x64_i8 v[90:93], v[114:117], v[192:195], v[90:93]
	s_waitcnt lgkmcnt(1)
	v_mfma_i32_16x16x64_i8 v[78:81], v[106:109], v[212:215], v[78:81]
	v_mfma_i32_16x16x64_i8 v[74:77], v[114:117], v[212:215], v[74:77]
	v_mfma_i32_16x16x64_i8 v[158:161], v[110:113], v[168:171], v[158:161]
	v_mfma_i32_16x16x64_i8 v[154:157], v[118:121], v[168:171], v[154:157]
	v_mfma_i32_16x16x64_i8 v[134:137], v[110:113], v[188:191], v[134:137]
	v_mfma_i32_16x16x64_i8 v[122:125], v[118:121], v[188:191], v[122:125]
	v_mfma_i32_16x16x64_i8 v[94:97], v[110:113], v[208:211], v[94:97]
	v_mfma_i32_16x16x64_i8 v[90:93], v[118:121], v[208:211], v[90:93]
	s_waitcnt lgkmcnt(0)
	v_mfma_i32_16x16x64_i8 v[78:81], v[110:113], v[216:219], v[78:81]
	v_mfma_i32_16x16x64_i8 v[74:77], v[118:121], v[216:219], v[74:77]
	s_setprio 0
	s_setprio 1
	v_mfma_i32_16x16x64_i8 v[150:153], v[126:129], v[164:167], v[150:153]
	v_mfma_i32_16x16x64_i8 v[146:149], v[138:141], v[164:167], v[146:149]
	v_mfma_i32_16x16x64_i8 v[102:105], v[126:129], v[184:187], v[102:105]
	v_mfma_i32_16x16x64_i8 v[98:101], v[138:141], v[184:187], v[98:101]
	v_mfma_i32_16x16x64_i8 v[86:89], v[126:129], v[192:195], v[86:89]
	v_mfma_i32_16x16x64_i8 v[82:85], v[138:141], v[192:195], v[82:85]
	v_mfma_i32_16x16x64_i8 v[70:73], v[126:129], v[212:215], v[70:73]
	v_mfma_i32_16x16x64_i8 v[66:69], v[138:141], v[212:215], v[66:69]
	v_mfma_i32_16x16x64_i8 v[150:153], v[130:133], v[168:171], v[150:153]
	v_mfma_i32_16x16x64_i8 v[146:149], v[142:145], v[168:171], v[146:149]
	v_mfma_i32_16x16x64_i8 v[102:105], v[130:133], v[188:191], v[102:105]
	v_mfma_i32_16x16x64_i8 v[98:101], v[142:145], v[188:191], v[98:101]
	v_mfma_i32_16x16x64_i8 v[86:89], v[130:133], v[208:211], v[86:89]
	v_mfma_i32_16x16x64_i8 v[82:85], v[142:145], v[208:211], v[82:85]
	v_mfma_i32_16x16x64_i8 v[70:73], v[130:133], v[216:219], v[70:73]
	v_mfma_i32_16x16x64_i8 v[66:69], v[142:145], v[216:219], v[66:69]
	s_setprio 0
	s_barrier
	s_mov_b32 s59, s85
	ds_read_b128 v[164:167], v178 offset:16384
	ds_read_b128 v[168:171], v178 offset:17408
	ds_read_b128 v[184:187], v178 offset:18432
	ds_read_b128 v[188:191], v178 offset:19456
	ds_read_b128 v[192:195], v178 offset:20480
	ds_read_b128 v[208:211], v178 offset:21504
	ds_read_b128 v[212:215], v178 offset:22528
	ds_read_b128 v[216:219], v178 offset:23552
	s_add_i32 m0, s59, 0x10000
	s_mov_b32 s59, s85
	buffer_load_dwordx4 v173, s[64:67], s53 offen lds
	s_add_i32 m0, s59, 0x12000
	s_mov_b32 s60, s85
	buffer_load_dwordx4 v175, s[64:67], s53 offen lds
	s_add_i32 s59, s53, 0x4000
	s_add_i32 m0, s60, 0x14000
	s_mov_b32 s60, s85
	buffer_load_dwordx4 v173, s[64:67], s59 offen lds
	s_add_i32 m0, s60, 0x16000
	s_nop 0
	buffer_load_dwordx4 v175, s[64:67], s59 offen lds
	s_mov_b32 s59, s85
	s_mov_b32 m0, s59
	s_mov_b32 s59, s85
	buffer_load_dwordx4 v172, s[88:91], s58 offen lds
	s_add_i32 m0, s59, 0x2000
	s_nop 0
	buffer_load_dwordx4 v174, s[88:91], s58 offen lds
	s_cmp_lg_u32 s55, 0
	s_cbranch_scc1 .Lgr17
	s_waitcnt vmcnt(8)

; #define PG8_STAGE(bufoff, RS, soff, voff) do { _Pragma("unroll") for (int _i = 0; _i < 2; ++_i) \
;         __builtin_amdgcn_raw_ptr_buffer_load_lds(RS, (PG8_LAS void*)(lds + (bufoff) + sgpr_opaque(ldsw) + _i * 8192), 16, (int)(voff)[_i], (int)(soff), 0, 0); } while (0)
; #define PG8_LDA(dst, b, h) do { _Pragma("unroll") for (int m = 0; m < 4; ++m) _Pragma("unroll") for (int k = 0; k < 2; ++k) dst[m][k] = *(const PG8_LAS f16x8*)(lds + PG8_SA(b, h) + aoff + m * 2048 + k * 1024); } while (0)
; #define PG8_LDB(dst, b, h) do { _Pragma("unroll") for (int n = 0; n < 2; ++n) _Pragma("unroll") for (int k = 0; k < 2; ++k) dst[n][k] = *(const PG8_LAS f16x8*)(lds + PG8_SB(b, h) + boff + n * 2048 + k * 1024); } while (0)
; #define PG8_WAIT_L(n) asm volatile("s_waitcnt lgkmcnt(" #n ")" ::: "memory")
; #define PG8_BAR __builtin_amdgcn_s_barrier()
; #define PG8_SCHED __builtin_amdgcn_sched_barrier(0)
; template <class Epi, class Sched, bool ALIGN_EPI = false, bool SP2 = false, bool I8 = false, bool ATILED = false>
; __device__ __forceinline__ void gemm_phase(PG8_LAS unsigned char* lds, const Gemm g, const Sched& S, const Epi& E, const int wid) {
;     ...
;             PG8_WAIT_VG; PG8_WAIT_L(0); PG8_BAR; PG8_MMA(1, 0, At, B0); PG8_MMA(1, 1, At, B1); PG8_BAR; PG8_SCHED;
;             PG8_LDB(B0, 1, 0); PG8_LDB(B1, 1, 1); PG8_SCHED; PG8_LDA(At, 1, 0); PG8_STAGE(PG8_SA(0, 1), rsA, a2 + hstepA, voffA);
;             PG8_WAIT_VG; PG8_WAIT_L(0); PG8_BAR; PG8_MMA(0, 0, At, B0); PG8_MMA(0, 1, At, B1); PG8_BAR; PG8_SCHED;
;             PG8_LDA(At, 1, 1); PG8_STAGE(PG8_SB(1, 0), rsB, b3, voffB); PG8_STAGE(PG8_SB(1, 1), rsB, b3 + hstep, voffB); PG8_STAGE(PG8_SA(1, 0), rsA, a3, voffA);
;             PG8_WAIT_VG; PG8_WAIT_L(0); PG8_BAR; PG8_MMA(1, 0, At, B0); PG8_MMA(1, 1, At, B1); PG8_BAR; PG8_SCHED;
.Lgr18:
	s_waitcnt vmcnt(24)
	s_waitcnt lgkmcnt(0)
	s_barrier
	s_setprio 1
	s_waitcnt lgkmcnt(7)
	v_mfma_i32_16x16x64_i8 v[158:161], v[106:109], v[164:167], v[158:161]
	v_mfma_i32_16x16x64_i8 v[154:157], v[114:117], v[164:167], v[154:157]
	s_waitcnt lgkmcnt(5)
	v_mfma_i32_16x16x64_i8 v[134:137], v[106:109], v[184:187], v[134:137]
	v_mfma_i32_16x16x64_i8 v[122:125], v[114:117], v[184:187], v[122:125]
	s_waitcnt lgkmcnt(3)
	v_mfma_i32_16x16x64_i8 v[94:97], v[106:109], v[192:195], v[94:97]
	v_mfma_i32_16x16x64_i8 v[90:93], v[114:117], v[192:195], v[90:93]
	s_waitcnt lgkmcnt(1)
	v_mfma_i32_16x16x64_i8 v[78:81], v[106:109], v[212:215], v[78:81]
	v_mfma_i32_16x16x64_i8 v[74:77], v[114:117], v[212:215], v[74:77]
	v_mfma_i32_16x16x64_i8 v[158:161], v[110:113], v[168:171], v[158:161]
	v_mfma_i32_16x16x64_i8 v[154:157], v[118:121], v[168:171], v[154:157]
	v_mfma_i32_16x16x64_i8 v[134:137], v[110:113], v[188:191], v[134:137]
	v_mfma_i32_16x16x64_i8 v[122:125], v[118:121], v[188:191], v[122:125]
	v_mfma_i32_16x16x64_i8 v[94:97], v[110:113], v[208:211], v[94:97]
	v_mfma_i32_16x16x64_i8 v[90:93], v[118:121], v[208:211], v[90:93]
	s_waitcnt lgkmcnt(0)
	v_mfma_i32_16x16x64_i8 v[78:81], v[110:113], v[216:219], v[78:81]
	v_mfma_i32_16x16x64_i8 v[74:77], v[118:121], v[216:219], v[74:77]
	s_setprio 0
	s_setprio 1
	v_mfma_i32_16x16x64_i8 v[150:153], v[126:129], v[164:167], v[150:153]
	v_mfma_i32_16x16x64_i8 v[146:149], v[138:141], v[164:167], v[146:149]
	v_mfma_i32_16x16x64_i8 v[102:105], v[126:129], v[184:187], v[102:105]
	v_mfma_i32_16x16x64_i8 v[98:101], v[138:141], v[184:187], v[98:101]
	v_mfma_i32_16x16x64_i8 v[86:89], v[126:129], v[192:195], v[86:89]
	v_mfma_i32_16x16x64_i8 v[82:85], v[138:141], v[192:195], v[82:85]
	v_mfma_i32_16x16x64_i8 v[70:73], v[126:129], v[212:215], v[70:73]
	v_mfma_i32_16x16x64_i8 v[66:69], v[138:141], v[212:215], v[66:69]
	v_mfma_i32_16x16x64_i8 v[150:153], v[130:133], v[168:171], v[150:153]
	v_mfma_i32_16x16x64_i8 v[146:149], v[142:145], v[168:171], v[146:149]
	v_mfma_i32_16x16x64_i8 v[102:105], v[130:133], v[188:191], v[102:105]
	v_mfma_i32_16x16x64_i8 v[98:101], v[142:145], v[188:191], v[98:101]
	v_mfma_i32_16x16x64_i8 v[86:89], v[130:133], v[208:211], v[86:89]
	v_mfma_i32_16x16x64_i8 v[82:85], v[142:145], v[208:211], v[82:85]
	v_mfma_i32_16x16x64_i8 v[70:73], v[130:133], v[216:219], v[70:73]
	v_mfma_i32_16x16x64_i8 v[66:69], v[142:145], v[216:219], v[66:69]
	s_setprio 0
	s_barrier
	s_mov_b32 s58, s85
	ds_read_b128 v[164:167], v178 offset:49152
	ds_read_b128 v[168:171], v178 offset:50176
	ds_read_b128 v[184:187], v178 offset:51200
	ds_read_b128 v[188:191], v178 offset:52224
	ds_read_b128 v[192:195], v178 offset:53248
	ds_read_b128 v[208:211], v178 offset:54272
	ds_read_b128 v[212:215], v178 offset:55296
	ds_read_b128 v[216:219], v178 offset:56320
	s_add_i32 m0, s58, 0x18000
	s_mov_b32 s58, s85
	buffer_load_dwordx4 v173, s[64:67], s54 offen lds
	s_add_i32 m0, s58, 0x1a000
	s_add_i32 s53, s53, 0xc000
	buffer_load_dwordx4 v175, s[64:67], s54 offen lds
	s_mov_b32 s54, s85
	s_add_i32 m0, s54, 0x1c000
	s_mov_b32 s54, s85
	buffer_load_dwordx4 v173, s[64:67], s53 offen lds
	s_add_i32 m0, s54, 0x1e000
	s_nop 0
	buffer_load_dwordx4 v175, s[64:67], s53 offen lds
	s_mov_b32 s53, s85
	s_add_i32 m0, s53, 0x8000
	s_mov_b32 s53, s85
	buffer_load_dwordx4 v172, s[88:91], s52 offen lds
	s_add_i32 m0, s53, 0xa000
	s_nop 0
	buffer_load_dwordx4 v174, s[88:91], s52 offen lds
	s_cmp_lg_u32 s55, 0
	s_cbranch_scc1 .Lgr19
	s_waitcnt vmcnt(8)
.Lgr19:
	s_waitcnt vmcnt(24)
	s_waitcnt lgkmcnt(0)
	s_barrier
	s_setprio 1
	s_waitcnt lgkmcnt(7)
	v_mfma_i32_16x16x64_i8 v[62:65], v[106:109], v[164:167], v[62:65]
	v_mfma_i32_16x16x64_i8 v[58:61], v[114:117], v[164:167], v[58:61]
	s_waitcnt lgkmcnt(5)
	v_mfma_i32_16x16x64_i8 v[46:49], v[106:109], v[184:187], v[46:49]
	v_mfma_i32_16x16x64_i8 v[42:45], v[114:117], v[184:187], v[42:45]
	s_waitcnt lgkmcnt(3)
	v_mfma_i32_16x16x64_i8 v[30:33], v[106:109], v[192:195], v[30:33]
	v_mfma_i32_16x16x64_i8 v[26:29], v[114:117], v[192:195], v[26:29]
	s_waitcnt lgkmcnt(1)
	v_mfma_i32_16x16x64_i8 v[14:17], v[106:109], v[212:215], v[14:17]
	v_mfma_i32_16x16x64_i8 v[10:13], v[114:117], v[212:215], v[10:13]
	v_mfma_i32_16x16x64_i8 v[62:65], v[110:113], v[168:171], v[62:65]
	v_mfma_i32_16x16x64_i8 v[58:61], v[118:121], v[168:171], v[58:61]
	v_mfma_i32_16x16x64_i8 v[46:49], v[110:113], v[188:191], v[46:49]
	v_mfma_i32_16x16x64_i8 v[42:45], v[118:121], v[188:191], v[42:45]
	v_mfma_i32_16x16x64_i8 v[30:33], v[110:113], v[208:211], v[30:33]
	v_mfma_i32_16x16x64_i8 v[26:29], v[118:121], v[208:211], v[26:29]
	s_waitcnt lgkmcnt(0)
	v_mfma_i32_16x16x64_i8 v[14:17], v[110:113], v[216:219], v[14:17]
	v_mfma_i32_16x16x64_i8 v[10:13], v[118:121], v[216:219], v[10:13]
	s_setprio 0
	s_setprio 1
	v_mfma_i32_16x16x64_i8 v[54:57], v[126:129], v[164:167], v[54:57]
	v_mfma_i32_16x16x64_i8 v[50:53], v[138:141], v[164:167], v[50:53]
	v_mfma_i32_16x16x64_i8 v[38:41], v[126:129], v[184:187], v[38:41]
	v_mfma_i32_16x16x64_i8 v[34:37], v[138:141], v[184:187], v[34:37]
	v_mfma_i32_16x16x64_i8 v[22:25], v[126:129], v[192:195], v[22:25]
	v_mfma_i32_16x16x64_i8 v[18:21], v[138:141], v[192:195], v[18:21]
	v_mfma_i32_16x16x64_i8 v[6:9], v[126:129], v[212:215], v[6:9]
	v_mfma_i32_16x16x64_i8 v[2:5], v[138:141], v[212:215], v[2:5]
	v_mfma_i32_16x16x64_i8 v[54:57], v[130:133], v[168:171], v[54:57]
	v_mfma_i32_16x16x64_i8 v[50:53], v[142:145], v[168:171], v[50:53]
	v_mfma_i32_16x16x64_i8 v[38:41], v[130:133], v[188:191], v[38:41]
	v_mfma_i32_16x16x64_i8 v[34:37], v[142:145], v[188:191], v[34:37]
	v_mfma_i32_16x16x64_i8 v[22:25], v[130:133], v[208:211], v[22:25]
	v_mfma_i32_16x16x64_i8 v[18:21], v[142:145], v[208:211], v[18:21]
	v_mfma_i32_16x16x64_i8 v[6:9], v[130:133], v[216:219], v[6:9]
	v_mfma_i32_16x16x64_i8 v[2:5], v[142:145], v[216:219], v[2:5]
	s_setprio 0
	s_barrier
	s_add_i32 s51, s51, 2
	s_addk_i32 s49, 0x100
	s_add_i32 s50, s50, 0x10000
	s_cmp_gt_u32 s51, 5
	s_cbranch_scc0 .LBB0_1611
	s_and_b64 vcc, exec, s[56:57]
	s_cbranch_vccz .LBB0_1614
	s_barrier

; __global__ void __launch_bounds__(NWAVES * 64, 2) mega_fwd(Args args) {
;     extern __shared__ __attribute__((aligned(16))) unsigned char lds_raw[];
	.amdhsa_kernel _Z8mega_fwd4Args
		.amdhsa_group_segment_fixed_size 0
		.amdhsa_private_segment_fixed_size 0
		.amdhsa_kernarg_size 432
		.amdhsa_user_sgpr_count 2
		.amdhsa_user_sgpr_dispatch_ptr 0
		.amdhsa_user_sgpr_queue_ptr 0
		.amdhsa_user_sgpr_kernarg_segment_ptr 1
		.amdhsa_user_sgpr_dispatch_id 0
		.amdhsa_user_sgpr_kernarg_preload_length 0
		.amdhsa_user_sgpr_kernarg_preload_offset 0
		.amdhsa_user_sgpr_private_segment_size 0
		.amdhsa_uses_dynamic_stack 0
		.amdhsa_enable_private_segment 0
		.amdhsa_system_sgpr_workgroup_id_x 1
		.amdhsa_system_sgpr_workgroup_id_y 0
		.amdhsa_system_sgpr_workgroup_id_z 0
		.amdhsa_system_sgpr_workgroup_info 0
		.amdhsa_system_vgpr_workitem_id 0
		.amdhsa_next_free_vgpr 256
		.amdhsa_next_free_sgpr 102
		.amdhsa_accum_offset 256
		.amdhsa_reserve_vcc 1
		.amdhsa_float_round_mode_32 0
		.amdhsa_float_round_mode_16_64 0
		.amdhsa_float_denorm_mode_32 3
		.amdhsa_float_denorm_mode_16_64 3
		.amdhsa_dx10_clamp 1
		.amdhsa_ieee_mode 1
		.amdhsa_fp16_overflow 0
		.amdhsa_tg_split 0
		.amdhsa_exception_fp_ieee_invalid_op 0
		.amdhsa_exception_fp_denorm_src 0
		.amdhsa_exception_fp_ieee_div_zero 0
		.amdhsa_exception_fp_ieee_overflow 0
		.amdhsa_exception_fp_ieee_underflow 0
		.amdhsa_exception_fp_ieee_inexact 0
		.amdhsa_exception_int_div_zero 0
	.end_amdhsa_kernel

; __global__ void __launch_bounds__(NWAVES * 64, 2) mega_fwd(Args args) {
amdhsa.kernels:
  - .agpr_count:     0
    .args:
      - .offset:         0
        .size:           176
        .value_kind:     by_value
      - .offset:         176
        .size:           4
        .value_kind:     hidden_block_count_x
      - .offset:         180
        .size:           4
        .value_kind:     hidden_block_count_y
      - .offset:         184
        .size:           4
        .value_kind:     hidden_block_count_z
      - .offset:         188
        .size:           2
        .value_kind:     hidden_group_size_x
      - .offset:         190
        .size:           2
        .value_kind:     hidden_group_size_y
      - .offset:         192
        .size:           2
        .value_kind:     hidden_group_size_z
      - .offset:         194
        .size:           2
        .value_kind:     hidden_remainder_x
      - .offset:         196
        .size:           2
        .value_kind:     hidden_remainder_y
      - .offset:         198
        .size:           2
        .value_kind:     hidden_remainder_z
      - .offset:         216
        .size:           8
        .value_kind:     hidden_global_offset_x
      - .offset:         224
        .size:           8
        .value_kind:     hidden_global_offset_y
      - .offset:         232
        .size:           8
        .value_kind:     hidden_global_offset_z
      - .offset:         240
        .size:           2
        .value_kind:     hidden_grid_dims
    .group_segment_fixed_size: 0
    .kernarg_segment_align: 8
    .kernarg_segment_size: 432
    .language:       OpenCL C
    .language_version:
      - 2
      - 0
    .max_flat_workgroup_size: 512
    .name:           _Z8mega_fwd4Args
    .private_segment_fixed_size: 0
    .sgpr_count:     108
    .sgpr_spill_count: 185
    .symbol:         _Z8mega_fwd4Args.kd
    .uniform_work_group_size: 1
    .uses_dynamic_stack: false
    .vgpr_count:     256
    .vgpr_spill_count: 0
    .wavefront_size: 64
